# s5_pass_c: next-tile A operand prefetched + epilogue u loads hoisted with counted vmcnt; MoE gate-up SwiGLU epilogue: folded constant muls, fma for (u+1)*4, no-op clamp and zero-init removed
# speedup vs baseline: 1.0070x; 1.0070x over previous
.LBB0_1002:
	v_mul_f32_e32 v2, v116, v124
	v_fma_f32 v105, -v117, v126, v2
	v_mul_f32_e32 v165, v116, v126
	v_mul_f32_e32 v2, v118, v125
	v_mul_f32_e32 v167, v118, v127
	s_lshl_b32 s0, s5, 8
	v_fmac_f32_e32 v165, v117, v124
	v_fma_f32 v166, -v119, v127, v2
	v_fmac_f32_e32 v167, v119, v125
	v_mov_b32_e32 v133, s7
	v_or_b32_e32 v132, s6, v102
	v_lshl_add_u64 v[136:137], s[6:7], 1, v[112:113]
	v_or_b32_e32 v168, s0, v1
	v_or_b32_e32 v169, s0, v156
	s_mov_b32 s0, 0
	v_ashrrev_i32_e32 v189, 31, v169
	v_mov_b32_e32 v188, v169
	v_lshlrev_b64 v[188:189], 11, v[188:189]
	v_lshl_add_u64 v[188:189], v[136:137], 0, v[188:189]
	global_load_dwordx4 v[180:183], v[188:189], off
	s_waitcnt vmcnt(0)
.LBB0_1003:
	v_pk_mul_f32 v[176:177], v[130:131], v[134:135]
	v_mfma_f32_32x32x16_bf16 v[34:49], v[180:183], v[66:69], 0
	v_fma_f32 v176, v128, v138, v176
	v_fma_f32 v177, v129, v139, v177
	s_nop 9
	v_mov_b32_e32 v140, v34
	v_mfma_f32_32x32x16_bf16 v[2:17], v[180:183], v[70:73], 0
	v_mov_b32_e32 v146, v35
	v_mov_b32_e32 v174, v44
	v_mov_b32_e32 v158, v38
	v_mfma_f32_32x32x16_bf16 v[50:65], v[180:183], v[74:77], 0
	s_nop 7
	v_mov_b32_e32 v141, v2
	v_mov_b32_e32 v147, v3
	v_mov_b32_e32 v175, v12
	v_mov_b32_e32 v159, v6
	v_mfma_f32_32x32x16_bf16 v[18:33], v[180:183], v[78:81], 0
	v_mov_b32_e32 v188, s0
	v_add_u32_e32 v188, 32, v188
	v_min_u32_e32 v188, 0xe0, v188
	v_add_u32_e32 v188, v188, v169
	v_ashrrev_i32_e32 v189, 31, v188
	v_lshlrev_b64 v[188:189], 11, v[188:189]
	v_lshl_add_u64 v[188:189], v[136:137], 0, v[188:189]
	global_load_dwordx4 v[180:183], v[188:189], off
	v_add_u32_e32 v190, s0, v168
	v_ashrrev_i32_e32 v191, 31, v190
	v_lshlrev_b64 v[190:191], 10, v[190:191]
	v_lshl_add_u64 v[190:191], v[190:191], 0, v[132:133]
	v_lshlrev_b64 v[190:191], 1, v[190:191]
	v_lshl_add_u64 v[190:191], s[22:23], 0, v[190:191]
	global_load_dwordx2 v[184:185], v[190:191], off
	v_add_u32_e32 v192, s0, v168
	v_add_u32_e32 v192, 16, v192
	v_ashrrev_i32_e32 v193, 31, v192
	v_lshlrev_b64 v[192:193], 10, v[192:193]
	v_lshl_add_u64 v[192:193], v[192:193], 0, v[132:133]
	v_lshlrev_b64 v[192:193], 1, v[192:193]
	v_lshl_add_u64 v[192:193], s[22:23], 0, v[192:193]
	global_load_dwordx2 v[186:187], v[192:193], off
	v_mov_b32_e32 v142, v50
	s_nop 10
	v_mov_b32_e32 v143, v18
	v_pk_mul_f32 v[144:145], v[122:123], v[142:143]
	v_pk_mul_f32 v[142:143], v[120:121], v[142:143]
	v_pk_fma_f32 v[144:145], v[120:121], v[140:141], v[144:145] neg_lo:[0,0,1] neg_hi:[0,0,1]
	v_pk_fma_f32 v[140:141], v[122:123], v[140:141], v[142:143]
	v_mov_b32_e32 v142, v51
	v_mov_b32_e32 v143, v19
	v_pk_add_f32 v[150:151], v[142:143], v[140:141]
	v_pk_add_f32 v[148:149], v[146:147], v[144:145]
	v_pk_mul_f32 v[140:141], v[122:123], v[150:151]
	v_mov_b32_e32 v142, v36
	v_pk_fma_f32 v[140:141], v[120:121], v[148:149], v[140:141] neg_lo:[0,0,1] neg_hi:[0,0,1]
	v_mov_b32_e32 v143, v4
	v_pk_add_f32 v[152:153], v[142:143], v[140:141]
	v_pk_mul_f32 v[140:141], v[122:123], v[148:149]
	v_mov_b32_e32 v142, v52
	v_pk_fma_f32 v[140:141], v[120:121], v[150:151], v[140:141]
	v_mov_b32_e32 v143, v20
	v_pk_add_f32 v[154:155], v[142:143], v[140:141]
	v_mov_b32_e32 v140, v54
	v_mov_b32_e32 v141, v22
	v_mov_b32_e32 v144, v58
	v_mov_b32_e32 v145, v26
	v_pk_mul_f32 v[160:161], v[122:123], v[140:141]
	v_pk_mul_f32 v[162:163], v[120:121], v[140:141]
	v_mov_b32_e32 v142, v42
	v_mov_b32_e32 v143, v10
	v_pk_mul_f32 v[140:141], v[122:123], v[144:145]
	v_mov_b32_e32 v146, v43
	v_pk_fma_f32 v[140:141], v[120:121], v[142:143], v[140:141] neg_lo:[0,0,1] neg_hi:[0,0,1]
	v_mov_b32_e32 v147, v11
	v_pk_mul_f32 v[144:145], v[120:121], v[144:145]
	v_pk_add_f32 v[140:141], v[146:147], v[140:141]
	v_pk_fma_f32 v[142:143], v[122:123], v[142:143], v[144:145]
	v_mov_b32_e32 v144, v59
	v_mov_b32_e32 v145, v27
	v_pk_mul_f32 v[172:173], v[122:123], v[154:155]
	v_pk_add_f32 v[142:143], v[144:145], v[142:143]
	v_pk_mul_f32 v[144:145], v[122:123], v[140:141]
	v_pk_fma_f32 v[172:173], v[120:121], v[152:153], v[172:173] neg_lo:[0,0,1] neg_hi:[0,0,1]
	v_pk_fma_f32 v[146:147], v[120:121], v[142:143], v[144:145]
	v_pk_mul_f32 v[144:145], v[122:123], v[142:143]
	v_mov_b32_e32 v4, v37
	v_pk_mul_f32 v[170:171], v[122:123], v[152:153]
	v_pk_fma_f32 v[144:145], v[120:121], v[140:141], v[144:145] neg_lo:[0,0,1] neg_hi:[0,0,1]
	v_pk_add_f32 v[4:5], v[4:5], v[172:173]
	v_pk_add_f32 v[144:145], v[174:175], v[144:145]
	v_mov_b32_e32 v175, v28
	v_mov_b32_e32 v3, v4
	v_mov_b32_e32 v11, v4
	v_pk_fma_f32 v[36:37], v[120:121], v[154:155], v[170:171]
	v_mov_b32_e32 v20, v53
	v_mov_b32_e32 v27, v5
	v_mov_b32_e32 v28, v5
	v_permlane32_swap_b32_e32 v3, v11
	v_pk_add_f32 v[20:21], v[20:21], v[36:37]
	v_permlane32_swap_b32_e32 v27, v28
	v_mov_b32_e32 v12, v20
	v_mov_b32_e32 v19, v20
	v_cndmask_b32_e32 v27, v27, v28, vcc
	v_cndmask_b32_e32 v3, v3, v11, vcc
	v_mov_b32_e32 v11, v21
	v_mov_b32_e32 v28, v21
	v_mov_b32_e32 v174, v60
	v_permlane32_swap_b32_e32 v12, v19
	v_permlane32_swap_b32_e32 v11, v28
	v_pk_add_f32 v[146:147], v[174:175], v[146:147]
	v_pk_mul_f32 v[174:175], v[130:131], v[138:139]
	v_cndmask_b32_e32 v11, v11, v28, vcc
	v_cndmask_b32_e32 v12, v12, v19, vcc
	v_pk_fma_f32 v[174:175], v[128:129], v[134:135], v[174:175] neg_lo:[0,0,1] neg_hi:[0,0,1]
	v_cndmask_b32_e32 v36, v3, v4, vcc
	v_cndmask_b32_e32 v52, v12, v20, vcc
	v_cndmask_b32_e32 v37, v27, v5, vcc
	v_cndmask_b32_e32 v53, v11, v21, vcc
	v_pk_add_f32 v[170:171], v[174:175], v[36:37]
	v_pk_add_f32 v[172:173], v[176:177], v[52:53]
	v_pk_fma_f32 v[36:37], v[120:121], v[158:159], v[160:161] neg_lo:[0,0,1] neg_hi:[0,0,1]
	v_pk_fma_f32 v[52:53], v[122:123], v[158:159], v[162:163]
	v_mov_b32_e32 v158, v39
	v_mov_b32_e32 v159, v7
	v_pk_add_f32 v[36:37], v[158:159], v[36:37]
	v_mov_b32_e32 v158, v55
	v_mov_b32_e32 v159, v23
	v_pk_add_f32 v[52:53], v[158:159], v[52:53]
	v_pk_mul_f32 v[160:161], v[122:123], v[36:37]
	v_pk_mul_f32 v[158:159], v[122:123], v[52:53]
	v_mov_b32_e32 v162, v40
	v_pk_fma_f32 v[158:159], v[120:121], v[36:37], v[158:159] neg_lo:[0,0,1] neg_hi:[0,0,1]
	v_mov_b32_e32 v163, v8
	v_pk_fma_f32 v[160:161], v[120:121], v[52:53], v[160:161]
	v_pk_add_f32 v[158:159], v[162:163], v[158:159]
	v_mov_b32_e32 v162, v56
	v_mov_b32_e32 v163, v24
	v_pk_add_f32 v[160:161], v[162:163], v[160:161]
	v_mov_b32_e32 v8, v41
	v_pk_mul_f32 v[40:41], v[122:123], v[158:159]
	v_mov_b32_e32 v24, v57
	v_pk_fma_f32 v[40:41], v[120:121], v[160:161], v[40:41]
	v_pk_mul_f32 v[162:163], v[122:123], v[160:161]
	v_pk_add_f32 v[24:25], v[24:25], v[40:41]
	v_pk_fma_f32 v[162:163], v[120:121], v[158:159], v[162:163] neg_lo:[0,0,1] neg_hi:[0,0,1]
	v_mov_b32_e32 v35, v24
	v_mov_b32_e32 v39, v24
	v_mov_b32_e32 v40, v25
	v_mov_b32_e32 v41, v25
	v_pk_add_f32 v[8:9], v[8:9], v[162:163]
	v_permlane32_swap_b32_e32 v35, v39
	v_permlane32_swap_b32_e32 v40, v41
	v_pk_mul_f32 v[174:175], v[128:129], v[172:173]
	v_mov_b32_e32 v7, v8
	v_mov_b32_e32 v23, v8
	v_cndmask_b32_e32 v43, v35, v39, vcc
	v_cndmask_b32_e32 v39, v40, v41, vcc
	v_cndmask_b32_e32 v40, v4, v3, vcc
	v_cndmask_b32_e32 v57, v21, v11, vcc
	v_cndmask_b32_e32 v56, v20, v12, vcc
	v_pk_mul_f32 v[162:163], v[130:131], v[172:173]
	v_pk_fma_f32 v[174:175], v[130:131], v[170:171], v[174:175]
	v_mov_b32_e32 v3, v9
	v_mov_b32_e32 v11, v9
	v_permlane32_swap_b32_e32 v7, v23
	v_cndmask_b32_e32 v41, v5, v27, vcc
	v_pk_fma_f32 v[162:163], v[128:129], v[170:171], v[162:163] neg_lo:[0,0,1] neg_hi:[0,0,1]
	v_pk_add_f32 v[56:57], v[56:57], v[174:175]
	v_permlane32_swap_b32_e32 v3, v11
	v_pk_add_f32 v[40:41], v[40:41], v[162:163]
	v_cndmask_b32_e32 v7, v7, v23, vcc
	v_cndmask_b32_e32 v3, v3, v11, vcc
	v_pk_mul_f32 v[174:175], v[130:131], v[56:57]
	v_cndmask_b32_e32 v163, v3, v9, vcc
	v_cndmask_b32_e32 v162, v7, v8, vcc
	v_pk_fma_f32 v[174:175], v[128:129], v[40:41], v[174:175] neg_lo:[0,0,1] neg_hi:[0,0,1]
	v_pk_mul_f32 v[176:177], v[130:131], v[40:41]
	v_cndmask_b32_e32 v28, v172, v138, vcc
	v_pk_add_f32 v[162:163], v[162:163], v[174:175]
	v_cndmask_b32_e32 v175, v39, v25, vcc
	v_cndmask_b32_e32 v174, v43, v24, vcc
	v_pk_fma_f32 v[176:177], v[128:129], v[56:57], v[176:177]
	v_cndmask_b32_e32 v19, v170, v134, vcc
	v_pk_add_f32 v[174:175], v[174:175], v[176:177]
	v_cndmask_b32_e32 v177, v9, v3, vcc
	v_mul_f32_e32 v3, v117, v28
	v_fma_f32 v3, v116, v19, -v3
	v_add_f32_e32 v3, v34, v3
	v_mul_f32_e32 v34, v165, v28
	v_fma_f32 v34, v105, v19, -v34
	v_mul_f32_e32 v23, v126, v28
	v_add_f32_e32 v59, v152, v34
	v_mul_f32_e32 v34, v130, v28
	v_cndmask_b32_e32 v11, v162, v40, vcc
	v_cndmask_b32_e32 v176, v8, v7, vcc
	v_mul_f32_e32 v7, v117, v19
	v_fma_f32 v23, v124, v19, -v23
	v_mul_f32_e32 v27, v126, v19
	v_mul_f32_e32 v35, v165, v19
	v_fma_f32 v34, v128, v19, -v34
	v_mul_f32_e32 v19, v130, v19
	v_cndmask_b32_e32 v12, v174, v56, vcc
	v_fmac_f32_e32 v7, v116, v28
	v_fmac_f32_e32 v27, v124, v28
	v_fmac_f32_e32 v35, v105, v28
	v_fmac_f32_e32 v19, v128, v28
	v_mul_f32_e32 v28, v117, v11
	v_fmac_f32_e32 v28, v116, v12
	v_add_f32_e32 v27, v150, v27
	v_add_f32_e32 v150, v54, v28
	v_mul_f32_e32 v28, v126, v12
	v_fma_f32 v28, v124, v11, -v28
	v_add_f32_e32 v36, v36, v28
	v_mul_f32_e32 v28, v165, v12
	v_add_f32_e32 v4, v4, v34
	v_mul_f32_e32 v34, v126, v11
	v_fma_f32 v28, v105, v11, -v28
	v_add_f32_e32 v19, v20, v19
	v_mul_f32_e32 v20, v117, v12
	v_fmac_f32_e32 v34, v124, v12
	v_add_f32_e32 v152, v158, v28
	v_mul_f32_e32 v28, v130, v12
	v_add_f32_e32 v7, v50, v7
	v_fma_f32 v20, v116, v11, -v20
	v_add_f32_e32 v52, v52, v34
	v_mul_f32_e32 v34, v165, v11
	v_fma_f32 v28, v128, v11, -v28
	v_mul_f32_e32 v11, v130, v11
	v_pk_mul_f32 v[50:51], v[122:123], v[146:147]
	v_fmac_f32_e32 v34, v105, v12
	v_fmac_f32_e32 v11, v128, v12
	v_pk_fma_f32 v[50:51], v[120:121], v[144:145], v[50:51] neg_lo:[0,0,1] neg_hi:[0,0,1]
	v_mov_b32_e32 v12, v45
	v_pk_mul_f32 v[44:45], v[122:123], v[144:145]
	v_add_f32_e32 v8, v8, v28
	v_cndmask_b32_e32 v172, v163, v41, vcc
	v_pk_mul_f32 v[40:41], v[130:131], v[162:163]
	v_pk_add_f32 v[12:13], v[12:13], v[50:51]
	v_pk_fma_f32 v[44:45], v[120:121], v[146:147], v[44:45]
	v_mov_b32_e32 v28, v61
	v_pk_mul_f32 v[178:179], v[130:131], v[174:175]
	v_add_f32_e32 v20, v38, v20
	v_add_f32_e32 v11, v24, v11
	v_cndmask_b32_e32 v39, v25, v39, vcc
	v_cndmask_b32_e32 v38, v24, v43, vcc
	v_pk_fma_f32 v[40:41], v[128:129], v[174:175], v[40:41]
	v_mov_b32_e32 v24, v12
	v_mov_b32_e32 v43, v12
	v_pk_add_f32 v[28:29], v[28:29], v[44:45]
	v_mov_b32_e32 v44, v13
	v_mov_b32_e32 v45, v13
	v_pk_fma_f32 v[178:179], v[128:129], v[162:163], v[178:179] neg_lo:[0,0,1] neg_hi:[0,0,1]
	v_pk_add_f32 v[38:39], v[38:39], v[40:41]
	v_permlane32_swap_b32_e32 v24, v43
	v_permlane32_swap_b32_e32 v44, v45
	v_pk_add_f32 v[176:177], v[176:177], v[178:179]
	v_pk_mul_f32 v[40:41], v[130:131], v[38:39]
	v_cndmask_b32_e32 v24, v24, v43, vcc
	v_cndmask_b32_e32 v43, v44, v45, vcc
	v_cndmask_b32_e32 v45, v43, v13, vcc
	v_cndmask_b32_e32 v44, v24, v12, vcc
	v_pk_fma_f32 v[40:41], v[128:129], v[176:177], v[40:41] neg_lo:[0,0,1] neg_hi:[0,0,1]
	v_mov_b32_e32 v50, v28
	v_mov_b32_e32 v51, v28
	v_pk_add_f32 v[40:41], v[44:45], v[40:41]
	v_mov_b32_e32 v44, v29
	v_mov_b32_e32 v45, v29
	v_permlane32_swap_b32_e32 v50, v51
	s_nop 0
	v_permlane32_swap_b32_e32 v44, v45
	v_add_f32_e32 v23, v148, v23
	v_add_f32_e32 v148, v154, v35
	v_add_f32_e32 v154, v160, v34
	v_cndmask_b32_e32 v158, v171, v135, vcc
	v_pk_mul_f32 v[34:35], v[130:131], v[176:177]
	v_cndmask_b32_e32 v134, v50, v51, vcc
	v_cndmask_b32_e32 v135, v44, v45, vcc
	v_cndmask_b32_e32 v45, v135, v29, vcc
	v_cndmask_b32_e32 v44, v134, v28, vcc
	v_pk_fma_f32 v[34:35], v[128:129], v[38:39], v[34:35]
	v_mov_b32_e32 v50, v62
	v_mov_b32_e32 v51, v30
	v_pk_add_f32 v[34:35], v[44:45], v[34:35]
	v_mov_b32_e32 v44, v46
	v_mov_b32_e32 v45, v14
	v_pk_mul_f32 v[54:55], v[122:123], v[50:51]
	v_pk_mul_f32 v[50:51], v[120:121], v[50:51]
	v_pk_fma_f32 v[54:55], v[120:121], v[44:45], v[54:55] neg_lo:[0,0,1] neg_hi:[0,0,1]
	v_pk_fma_f32 v[44:45], v[122:123], v[44:45], v[50:51]
	v_mov_b32_e32 v50, v47
	v_mov_b32_e32 v51, v15
	v_pk_add_f32 v[50:51], v[50:51], v[54:55]
	v_mov_b32_e32 v54, v63
	v_mov_b32_e32 v55, v31
	v_pk_add_f32 v[44:45], v[54:55], v[44:45]
	v_cndmask_b32_e32 v160, v173, v139, vcc
	v_pk_mul_f32 v[54:55], v[122:123], v[44:45]
	v_cndmask_b32_e32 v173, v175, v57, vcc
	v_pk_fma_f32 v[54:55], v[120:121], v[50:51], v[54:55] neg_lo:[0,0,1] neg_hi:[0,0,1]
	v_pk_mul_f32 v[56:57], v[122:123], v[50:51]
	v_mov_b32_e32 v60, v48
	v_mov_b32_e32 v61, v16
	v_pk_fma_f32 v[56:57], v[120:121], v[44:45], v[56:57]
	v_pk_add_f32 v[54:55], v[60:61], v[54:55]
	v_mov_b32_e32 v60, v64
	v_mov_b32_e32 v61, v32
	v_pk_add_f32 v[56:57], v[60:61], v[56:57]
	v_mov_b32_e32 v16, v49
	v_pk_mul_f32 v[60:61], v[122:123], v[56:57]
	v_pk_mul_f32 v[48:49], v[122:123], v[54:55]
	v_pk_fma_f32 v[60:61], v[120:121], v[54:55], v[60:61] neg_lo:[0,0,1] neg_hi:[0,0,1]
	v_pk_fma_f32 v[48:49], v[120:121], v[56:57], v[48:49]
	v_pk_add_f32 v[16:17], v[16:17], v[60:61]
	v_mov_b32_e32 v32, v65
	v_mov_b32_e32 v15, v16
	v_mov_b32_e32 v31, v16
	v_pk_add_f32 v[32:33], v[32:33], v[48:49]
	v_mov_b32_e32 v48, v17
	v_mov_b32_e32 v49, v17
	v_cndmask_b32_e32 v61, v29, v135, vcc
	v_cndmask_b32_e32 v60, v28, v134, vcc
	v_pk_mul_f32 v[134:135], v[130:131], v[40:41]
	v_permlane32_swap_b32_e32 v15, v31
	v_permlane32_swap_b32_e32 v48, v49
	v_pk_mul_f32 v[64:65], v[130:131], v[34:35]
	v_pk_fma_f32 v[134:135], v[128:129], v[34:35], v[134:135]
	v_cndmask_b32_e32 v38, v34, v38, vcc
	v_mov_b32_e32 v47, v32
	v_mov_b32_e32 v63, v32
	v_cndmask_b32_e32 v15, v15, v31, vcc
	v_cndmask_b32_e32 v31, v48, v49, vcc
	v_cndmask_b32_e32 v49, v13, v43, vcc
	v_cndmask_b32_e32 v48, v12, v24, vcc
	v_pk_fma_f32 v[64:65], v[128:129], v[40:41], v[64:65] neg_lo:[0,0,1] neg_hi:[0,0,1]
	v_pk_add_f32 v[60:61], v[60:61], v[134:135]
	v_mov_b32_e32 v24, v33
	v_mov_b32_e32 v34, v33
	v_permlane32_swap_b32_e32 v47, v63
	v_pk_add_f32 v[48:49], v[48:49], v[64:65]
	v_pk_mul_f32 v[134:135], v[130:131], v[60:61]
	v_permlane32_swap_b32_e32 v24, v34
	v_cndmask_b32_e32 v174, v40, v176, vcc
	v_cndmask_b32_e32 v65, v31, v17, vcc
	v_cndmask_b32_e32 v64, v15, v16, vcc
	v_pk_fma_f32 v[134:135], v[128:129], v[48:49], v[134:135] neg_lo:[0,0,1] neg_hi:[0,0,1]
	v_cndmask_b32_e32 v40, v47, v63, vcc
	v_cndmask_b32_e32 v24, v24, v34, vcc
	v_pk_mul_f32 v[138:139], v[130:131], v[48:49]
	v_pk_add_f32 v[64:65], v[64:65], v[134:135]
	v_cndmask_b32_e32 v135, v24, v33, vcc
	v_cndmask_b32_e32 v134, v40, v32, vcc
	v_pk_fma_f32 v[138:139], v[128:129], v[60:61], v[138:139]
	v_mul_f32_e32 v43, v117, v174
	v_pk_add_f32 v[162:163], v[134:135], v[138:139]
	v_cndmask_b32_e32 v138, v32, v40, vcc
	v_mul_f32_e32 v40, v117, v38
	v_fma_f32 v40, v116, v174, -v40
	v_fmac_f32_e32 v43, v116, v38
	v_cvt_pk_bf16_f32 v3, v3, v3
	v_cndmask_b32_e32 v34, v162, v60, vcc
	v_add_f32_e32 v40, v42, v40
	v_add_f32_e32 v42, v58, v43
	v_mul_f32_e32 v47, v126, v174
	v_mul_f32_e32 v58, v165, v174
	v_mul_f32_e32 v63, v130, v174
	ds_write_b16 v157, v3
	v_cvt_pk_bf16_f32 v3, v23, v23
	v_cndmask_b32_e32 v139, v33, v24, vcc
	v_cndmask_b32_e32 v24, v64, v48, vcc
	v_mul_f32_e32 v43, v126, v38
	v_fmac_f32_e32 v47, v124, v38
	v_mul_f32_e32 v48, v165, v38
	v_fmac_f32_e32 v58, v105, v38
	v_mul_f32_e32 v60, v130, v38
	v_fmac_f32_e32 v63, v128, v38
	v_mul_f32_e32 v38, v117, v34
	ds_write_b16 v157, v3 offset:272
	v_cvt_pk_bf16_f32 v3, v59, v59
	v_fma_f32 v38, v116, v24, -v38
	ds_write_b16 v157, v3 offset:544
	v_cvt_pk_bf16_f32 v3, v4, v4
	v_fma_f32 v60, v128, v174, -v60
	v_add_f32_e32 v46, v46, v38
	v_mul_f32_e32 v38, v126, v34
	ds_write_b16 v157, v3 offset:816
	v_cvt_pk_bf16_f32 v3, v20, v20
	v_add_f32_e32 v12, v12, v60
	v_mul_f32_e32 v60, v117, v24
	v_fma_f32 v38, v124, v24, -v38
	ds_write_b16 v157, v3 offset:2176
	v_cvt_pk_bf16_f32 v3, v36, v36
	v_fmac_f32_e32 v60, v116, v34
	v_add_f32_e32 v50, v50, v38
	v_mul_f32_e32 v38, v165, v34
	ds_write_b16 v157, v3 offset:2448
	v_cvt_pk_bf16_f32 v3, v152, v152
	v_add_f32_e32 v60, v62, v60
	v_mul_f32_e32 v62, v126, v24
	v_fma_f32 v38, v105, v24, -v38
	ds_write_b16 v157, v3 offset:2720
	v_cvt_pk_bf16_f32 v3, v8, v8
	v_fma_f32 v43, v124, v174, -v43
	v_fmac_f32_e32 v62, v124, v34
	v_add_f32_e32 v54, v54, v38
	v_mul_f32_e32 v38, v130, v34
	ds_write_b16 v157, v3 offset:2992
	v_cvt_pk_bf16_f32 v3, v40, v40
	v_add_f32_e32 v43, v140, v43
	v_fma_f32 v48, v105, v174, -v48
	v_add_f32_e32 v44, v44, v62
	v_mul_f32_e32 v62, v165, v24
	v_fma_f32 v38, v128, v24, -v38
	v_mul_f32_e32 v24, v130, v24
	ds_write_b16 v157, v3 offset:4352
	v_cvt_pk_bf16_f32 v3, v43, v43
	v_add_f32_e32 v48, v144, v48
	v_fmac_f32_e32 v62, v105, v34
	v_fmac_f32_e32 v24, v128, v34
	ds_write_b16 v157, v3 offset:4624
	v_cvt_pk_bf16_f32 v3, v48, v48
	v_add_f32_e32 v56, v56, v62
	v_add_f32_e32 v62, v16, v38
	v_add_f32_e32 v24, v32, v24
	v_cndmask_b32_e32 v32, v41, v177, vcc
	v_cndmask_b32_e32 v41, v35, v39, vcc
	v_pk_mul_f32 v[38:39], v[130:131], v[162:163]
	ds_write_b16 v157, v3 offset:4896
	v_cvt_pk_bf16_f32 v3, v12, v12
	v_pk_mul_f32 v[134:135], v[130:131], v[64:65]
	v_cndmask_b32_e32 v35, v17, v31, vcc
	v_cndmask_b32_e32 v34, v16, v15, vcc
	v_pk_fma_f32 v[38:39], v[128:129], v[64:65], v[38:39] neg_lo:[0,0,1] neg_hi:[0,0,1]
	v_mul_f32_e32 v31, v119, v160
	ds_write_b16 v157, v3 offset:5168
	v_cvt_pk_bf16_f32 v3, v46, v46
	v_pk_fma_f32 v[170:171], v[128:129], v[162:163], v[134:135]
	v_pk_add_f32 v[134:135], v[34:35], v[38:39]
	v_cndmask_b32_e32 v15, v65, v49, vcc
	v_fma_f32 v31, v118, v158, -v31
	v_mul_f32_e32 v39, v131, v160
	v_mul_f32_e32 v49, v129, v160
	ds_write_b16 v157, v3 offset:6528
	v_cvt_pk_bf16_f32 v3, v50, v50
	v_add_f32_e32 v2, v2, v31
	v_mul_f32_e32 v31, v127, v160
	v_fma_f32 v39, v129, v158, -v39
	v_fmac_f32_e32 v49, v131, v158
	ds_write_b16 v157, v3 offset:6800
	v_cvt_pk_bf16_f32 v3, v54, v54
	v_fma_f32 v31, v125, v158, -v31
	v_mul_f32_e32 v35, v167, v160
	v_add_f32_e32 v5, v5, v39
	v_add_f32_e32 v21, v21, v49
	v_mul_f32_e32 v39, v119, v173
	v_mul_f32_e32 v49, v119, v172
	ds_write_b16 v157, v3 offset:7072
	v_cvt_pk_bf16_f32 v3, v62, v62
	ds_write_b16 v157, v3 offset:7344
	v_cvt_pk_bf16_f32 v2, v2, v2
	v_cndmask_b32_e32 v16, v163, v61, vcc
	v_add_f32_e32 v31, v149, v31
	v_fma_f32 v35, v166, v158, -v35
	v_fma_f32 v39, v118, v172, -v39
	v_fmac_f32_e32 v49, v118, v173
	v_mul_f32_e32 v61, v131, v173
	ds_write_b16 v157, v2 offset:64
	v_cvt_pk_bf16_f32 v2, v31, v31
	v_add_f32_e32 v28, v28, v63
	v_add_f32_e32 v35, v153, v35
	v_add_f32_e32 v6, v6, v39
	v_add_f32_e32 v22, v22, v49
	v_mul_f32_e32 v39, v127, v173
	v_mul_f32_e32 v49, v127, v172
	v_fma_f32 v61, v129, v172, -v61
	v_mul_f32_e32 v63, v131, v172
	ds_write_b16 v157, v2 offset:336
	v_cvt_pk_bf16_f32 v2, v35, v35
	v_fma_f32 v39, v125, v172, -v39
	v_fmac_f32_e32 v49, v125, v173
	v_fmac_f32_e32 v63, v129, v173
	v_add_f32_e32 v9, v9, v61
	v_mul_f32_e32 v61, v119, v41
	ds_write_b16 v157, v2 offset:608
	v_cvt_pk_bf16_f32 v2, v5, v5
	v_add_f32_e32 v37, v37, v39
	v_add_f32_e32 v39, v53, v49
	v_mul_f32_e32 v49, v167, v173
	v_add_f32_e32 v25, v25, v63
	v_fma_f32 v61, v118, v32, -v61
	v_mul_f32_e32 v63, v119, v32
	ds_write_b16 v157, v2 offset:880
	v_cvt_pk_bf16_f32 v2, v6, v6
	v_fma_f32 v49, v166, v172, -v49
	v_fmac_f32_e32 v63, v118, v41
	v_add_f32_e32 v10, v10, v61
	v_mul_f32_e32 v61, v127, v41
	v_mul_f32_e32 v64, v167, v41
	v_mul_f32_e32 v140, v131, v41
	ds_write_b16 v157, v2 offset:2240
	v_cvt_pk_bf16_f32 v2, v37, v37
	v_add_f32_e32 v49, v159, v49
	v_add_f32_e32 v26, v26, v63
	v_fma_f32 v61, v125, v32, -v61
	v_mul_f32_e32 v63, v127, v32
	v_fma_f32 v64, v166, v32, -v64
	v_mul_f32_e32 v65, v167, v32
	v_fma_f32 v140, v129, v32, -v140
	v_mul_f32_e32 v32, v131, v32
	ds_write_b16 v157, v2 offset:2512
	v_cvt_pk_bf16_f32 v2, v49, v49
	v_fmac_f32_e32 v63, v125, v41
	v_fmac_f32_e32 v65, v166, v41
	v_fmac_f32_e32 v32, v129, v41
	v_mul_f32_e32 v41, v119, v15
	ds_write_b16 v157, v2 offset:2784
	v_cvt_pk_bf16_f32 v2, v9, v9
	v_fmac_f32_e32 v41, v118, v16
	ds_write_b16 v157, v2 offset:3056
	v_cvt_pk_bf16_f32 v2, v10, v10
	v_add_f32_e32 v61, v141, v61
	v_add_f32_e32 v29, v29, v32
	v_mul_f32_e32 v32, v119, v16
	v_add_f32_e32 v30, v30, v41
	v_mul_f32_e32 v41, v127, v15
	ds_write_b16 v157, v2 offset:4416
	v_cvt_pk_bf16_f32 v2, v61, v61
	v_add_f32_e32 v64, v145, v64
	v_fma_f32 v32, v118, v15, -v32
	v_fmac_f32_e32 v41, v125, v16
	ds_write_b16 v157, v2 offset:4688
	v_cvt_pk_bf16_f32 v2, v64, v64
	v_add_f32_e32 v13, v13, v140
	v_add_f32_e32 v14, v14, v32
	v_mul_f32_e32 v32, v127, v16
	v_add_f32_e32 v41, v45, v41
	v_mul_f32_e32 v45, v167, v16
	ds_write_b16 v157, v2 offset:4960
	v_cvt_pk_bf16_f32 v2, v13, v13
	v_fma_f32 v32, v125, v15, -v32
	v_fma_f32 v45, v166, v15, -v45
	ds_write_b16 v157, v2 offset:5232
	v_cvt_pk_bf16_f32 v2, v14, v14
	v_add_f32_e32 v32, v51, v32
	v_add_f32_e32 v45, v55, v45
	v_mul_f32_e32 v55, v131, v16
	ds_write_b16 v157, v2 offset:6592
	v_cvt_pk_bf16_f32 v2, v32, v32
	v_mul_f32_e32 v51, v167, v15
	v_fma_f32 v55, v129, v15, -v55
	v_mul_f32_e32 v15, v131, v15
	ds_write_b16 v157, v2 offset:6864
	v_cvt_pk_bf16_f32 v2, v45, v45
	v_fmac_f32_e32 v51, v166, v16
	v_fmac_f32_e32 v15, v129, v16
	v_add_f32_e32 v16, v17, v55
	ds_write_b16 v157, v2 offset:7136
	v_cvt_pk_bf16_f32 v2, v16, v16
	ds_write_b16 v157, v2 offset:7408
	v_cvt_pk_bf16_f32 v2, v7, v7
	ds_write_b16 v157, v2 offset:128
	v_cvt_pk_bf16_f32 v2, v27, v27
	ds_write_b16 v157, v2 offset:400
	v_cvt_pk_bf16_f32 v2, v148, v148
	ds_write_b16 v157, v2 offset:672
	v_cvt_pk_bf16_f32 v2, v19, v19
	ds_write_b16 v157, v2 offset:944
	v_cvt_pk_bf16_f32 v2, v150, v150
	ds_write_b16 v157, v2 offset:2304
	v_cvt_pk_bf16_f32 v2, v52, v52
	ds_write_b16 v157, v2 offset:2576
	v_cvt_pk_bf16_f32 v2, v154, v154
	ds_write_b16 v157, v2 offset:2848
	v_cvt_pk_bf16_f32 v2, v11, v11
	ds_write_b16 v157, v2 offset:3120
	v_cvt_pk_bf16_f32 v2, v42, v42
	v_add_f32_e32 v47, v142, v47
	ds_write_b16 v157, v2 offset:4480
	v_cvt_pk_bf16_f32 v2, v47, v47
	v_add_f32_e32 v58, v146, v58
	ds_write_b16 v157, v2 offset:4752
	v_cvt_pk_bf16_f32 v2, v58, v58
	ds_write_b16 v157, v2 offset:5024
	v_cvt_pk_bf16_f32 v2, v28, v28
	ds_write_b16 v157, v2 offset:5296
	v_cvt_pk_bf16_f32 v2, v60, v60
	v_mul_f32_e32 v34, v118, v160
	ds_write_b16 v157, v2 offset:6656
	v_cvt_pk_bf16_f32 v2, v44, v44
	v_fmac_f32_e32 v34, v119, v158
	ds_write_b16 v157, v2 offset:6928
	v_cvt_pk_bf16_f32 v2, v56, v56
	v_add_f32_e32 v18, v18, v34
	v_mul_f32_e32 v34, v125, v160
	ds_write_b16 v157, v2 offset:7200
	v_cvt_pk_bf16_f32 v2, v24, v24
	v_fmac_f32_e32 v34, v127, v158
	v_mul_f32_e32 v38, v166, v160
	ds_write_b16 v157, v2 offset:7472
	v_cvt_pk_bf16_f32 v2, v18, v18
	v_add_f32_e32 v34, v151, v34
	v_fmac_f32_e32 v38, v167, v158
	ds_write_b16 v157, v2 offset:192
	v_cvt_pk_bf16_f32 v2, v34, v34
	v_add_f32_e32 v38, v155, v38
	ds_write_b16 v157, v2 offset:464
	v_cvt_pk_bf16_f32 v2, v38, v38
	ds_write_b16 v157, v2 offset:736
	v_cvt_pk_bf16_f32 v2, v21, v21
	v_mul_f32_e32 v53, v167, v172
	ds_write_b16 v157, v2 offset:1008
	v_cvt_pk_bf16_f32 v2, v22, v22
	v_fmac_f32_e32 v53, v166, v173
	ds_write_b16 v157, v2 offset:2368
	v_cvt_pk_bf16_f32 v2, v39, v39
	v_add_f32_e32 v53, v161, v53
	ds_write_b16 v157, v2 offset:2640
	v_cvt_pk_bf16_f32 v2, v53, v53
	ds_write_b16 v157, v2 offset:2912
	v_cvt_pk_bf16_f32 v2, v25, v25
	ds_write_b16 v157, v2 offset:3184
	v_cvt_pk_bf16_f32 v2, v26, v26
	v_add_f32_e32 v63, v143, v63
	ds_write_b16 v157, v2 offset:4544
	v_cvt_pk_bf16_f32 v2, v63, v63
	v_add_f32_e32 v65, v147, v65
	ds_write_b16 v157, v2 offset:4816
	v_cvt_pk_bf16_f32 v2, v65, v65
	ds_write_b16 v157, v2 offset:5088
	v_cvt_pk_bf16_f32 v2, v29, v29
	ds_write_b16 v157, v2 offset:5360
	v_cvt_pk_bf16_f32 v2, v30, v30
	ds_write_b16 v157, v2 offset:6720
	v_cvt_pk_bf16_f32 v2, v41, v41
	v_add_f32_e32 v51, v57, v51
	ds_write_b16 v157, v2 offset:6992
	v_cvt_pk_bf16_f32 v2, v51, v51
	v_add_f32_e32 v15, v33, v15
	ds_write_b16 v157, v2 offset:7264
	v_cvt_pk_bf16_f32 v2, v15, v15
	ds_write_b16 v157, v2 offset:7536
	s_waitcnt lgkmcnt(0)
	ds_read_b128 v[2:5], v164
	ds_read_b128 v[8:11], v164 offset:64
	s_waitcnt lgkmcnt(1)
	v_mfma_f32_16x16x32_bf16 v[2:5], v[82:85], v[2:5], 0
	v_add_u32_e32 v6, s0, v168
	v_ashrrev_i32_e32 v7, 31, v6
	s_add_i32 s0, s0, 32
	s_waitcnt lgkmcnt(0)
	v_mfma_f32_16x16x32_bf16 v[2:5], v[86:89], v[8:11], v[2:5]
	ds_read_b128 v[8:11], v164 offset:128
	v_pk_add_f32 v[138:139], v[138:139], v[170:171]
	s_cmpk_eq_i32 s0, 0x100
	s_waitcnt lgkmcnt(0)
	v_mfma_f32_16x16x32_bf16 v[2:5], v[90:93], v[8:11], v[2:5]
	ds_read_b128 v[8:11], v164 offset:192
	s_waitcnt lgkmcnt(0)
	v_mfma_f32_16x16x32_bf16 v[2:5], v[94:97], v[8:11], v[2:5]
	v_lshlrev_b64 v[8:9], 10, v[6:7]
	v_lshl_add_u64 v[8:9], v[8:9], 0, v[132:133]
	v_lshlrev_b64 v[8:9], 1, v[8:9]
	s_nop 1
	v_add_u32_e32 v6, 16, v6
	s_waitcnt vmcnt(1)
	v_lshlrev_b32_e32 v7, 16, v184
	v_fma_f32 v2, v98, v7, v2
	v_and_b32_e32 v7, 0xffff0000, v184
	v_fma_f32 v3, v99, v7, v3
	v_lshlrev_b32_e32 v7, 16, v185
	v_fma_f32 v4, v100, v7, v4
	v_and_b32_e32 v7, 0xffff0000, v185
	v_fmac_f32_e32 v5, v101, v7
	v_mul_f32_e32 v7, 0x3d372713, v2
	v_mul_f32_e32 v7, v2, v7
	v_fma_f32 v7, v2, v7, v2
	v_mul_f32_e32 v7, 0x3f4c422a, v7
	v_add_f32_e32 v7, v7, v7
	v_mul_f32_e32 v7, 0xbfb8aa3b, v7
	v_exp_f32_e32 v7, v7
	s_nop 0
	v_add_f32_e32 v7, 1.0, v7
	v_rcp_f32_e32 v7, v7
	s_nop 0
	v_mul_f32_e32 v2, v2, v7
	v_mul_f32_e32 v7, 0x3d372713, v3
	v_mul_f32_e32 v7, v3, v7
	v_fma_f32 v7, v3, v7, v3
	v_mul_f32_e32 v7, 0x3f4c422a, v7
	v_add_f32_e32 v7, v7, v7
	v_mul_f32_e32 v7, 0xbfb8aa3b, v7
	v_exp_f32_e32 v7, v7
	s_nop 0
	v_add_f32_e32 v7, 1.0, v7
	v_rcp_f32_e32 v7, v7
	s_nop 0
	v_mul_f32_e32 v3, v3, v7
	v_cvt_pk_bf16_f32 v2, v2, v3
	v_mul_f32_e32 v3, 0x3d372713, v4
	v_mul_f32_e32 v3, v4, v3
	v_fma_f32 v3, v4, v3, v4
	v_mul_f32_e32 v3, 0x3f4c422a, v3
	v_add_f32_e32 v3, v3, v3
	v_mul_f32_e32 v3, 0xbfb8aa3b, v3
	v_exp_f32_e32 v3, v3
	v_ashrrev_i32_e32 v7, 31, v6
	v_lshlrev_b64 v[6:7], 10, v[6:7]
	v_lshl_add_u64 v[6:7], v[6:7], 0, v[132:133]
	v_add_f32_e32 v3, 1.0, v3
	v_rcp_f32_e32 v3, v3
	v_lshlrev_b64 v[6:7], 1, v[6:7]
	v_mul_f32_e32 v3, v4, v3
	v_mul_f32_e32 v4, 0x3d372713, v5
	v_mul_f32_e32 v4, v5, v4
	v_fma_f32 v4, v5, v4, v5
	v_mul_f32_e32 v4, 0x3f4c422a, v4
	v_add_f32_e32 v4, v4, v4
	v_mul_f32_e32 v4, 0xbfb8aa3b, v4
	v_exp_f32_e32 v4, v4
	s_nop 0
	v_add_f32_e32 v4, 1.0, v4
	v_rcp_f32_e32 v4, v4
	s_nop 0
	v_mul_f32_e32 v4, v5, v4
	v_cvt_pk_bf16_f32 v3, v3, v4
	v_lshl_add_u64 v[4:5], s[90:91], 0, v[8:9]
	global_store_dwordx2 v[4:5], v[2:3], off
	ds_read_b128 v[2:5], v164 offset:4352
	ds_read_b128 v[8:11], v164 offset:4416
	s_waitcnt lgkmcnt(1)
	v_mfma_f32_16x16x32_bf16 v[2:5], v[82:85], v[2:5], 0
	s_waitcnt lgkmcnt(0)
	v_mfma_f32_16x16x32_bf16 v[2:5], v[86:89], v[8:11], v[2:5]
	ds_read_b128 v[8:11], v164 offset:4480
	s_waitcnt lgkmcnt(0)
	v_mfma_f32_16x16x32_bf16 v[2:5], v[90:93], v[8:11], v[2:5]
	ds_read_b128 v[8:11], v164 offset:4544
	s_waitcnt lgkmcnt(0)
	v_mfma_f32_16x16x32_bf16 v[2:5], v[94:97], v[8:11], v[2:5]
	s_nop 1
	s_waitcnt vmcnt(1)
	v_lshlrev_b32_e32 v10, 16, v186
	v_and_b32_e32 v8, 0xffff0000, v186
	s_nop 2
	v_fma_f32 v3, v99, v8, v3
	v_lshlrev_b32_e32 v8, 16, v187
	v_fma_f32 v2, v98, v10, v2
	v_fma_f32 v4, v100, v8, v4
	v_and_b32_e32 v8, 0xffff0000, v187
	v_fmac_f32_e32 v5, v101, v8
	v_mul_f32_e32 v8, 0x3d372713, v2
	v_mul_f32_e32 v8, v2, v8
	v_fma_f32 v8, v2, v8, v2
	v_mul_f32_e32 v8, 0x3f4c422a, v8
	v_add_f32_e32 v8, v8, v8
	v_mul_f32_e32 v8, 0xbfb8aa3b, v8
	v_exp_f32_e32 v8, v8
	s_nop 0
	v_add_f32_e32 v8, 1.0, v8
	v_rcp_f32_e32 v8, v8
	s_nop 0
	v_mul_f32_e32 v2, v2, v8
	v_mul_f32_e32 v8, 0x3d372713, v3
	v_mul_f32_e32 v8, v3, v8
	v_fma_f32 v8, v3, v8, v3
	v_mul_f32_e32 v8, 0x3f4c422a, v8
	v_add_f32_e32 v8, v8, v8
	v_mul_f32_e32 v8, 0xbfb8aa3b, v8
	v_exp_f32_e32 v8, v8
	s_nop 0
	v_add_f32_e32 v8, 1.0, v8
	v_rcp_f32_e32 v8, v8
	s_nop 0
	v_mul_f32_e32 v3, v3, v8
	v_cvt_pk_bf16_f32 v2, v2, v3
	v_mul_f32_e32 v3, 0x3d372713, v4
	v_mul_f32_e32 v3, v4, v3
	v_fma_f32 v3, v4, v3, v4
	v_mul_f32_e32 v3, 0x3f4c422a, v3
	v_add_f32_e32 v3, v3, v3
	v_mul_f32_e32 v3, 0xbfb8aa3b, v3
	v_exp_f32_e32 v3, v3
	s_nop 0
	v_add_f32_e32 v3, 1.0, v3
	v_rcp_f32_e32 v3, v3
	s_nop 0
	v_mul_f32_e32 v3, v4, v3
	v_mul_f32_e32 v4, 0x3d372713, v5
	v_mul_f32_e32 v4, v5, v4
	v_fma_f32 v4, v5, v4, v5
	v_mul_f32_e32 v4, 0x3f4c422a, v4
	v_add_f32_e32 v4, v4, v4
	v_mul_f32_e32 v4, 0xbfb8aa3b, v4
	v_exp_f32_e32 v4, v4
	s_nop 0
	v_add_f32_e32 v4, 1.0, v4
	v_rcp_f32_e32 v4, v4
	s_nop 0
	v_mul_f32_e32 v4, v5, v4
	v_cvt_pk_bf16_f32 v3, v3, v4
	v_lshl_add_u64 v[4:5], s[90:91], 0, v[6:7]
	global_store_dwordx2 v[4:5], v[2:3], off
	s_waitcnt lgkmcnt(0)
	s_cbranch_scc0 .LBB0_1003
	s_add_i32 s8, s8, s92
	s_cmpk_gt_i32 s8, 0xfff
	s_cbranch_scc0 .LBB0_989

.LBB0_2534:
	s_ashr_i32 s31, s30, 31
	v_readlane_b32 s60, v237, 29
	s_lshl_b64 s[6:7], s[30:31], 14
	v_readlane_b32 s62, v237, 31
	v_lshl_or_b32 v18, s28, 7, v188
	v_readlane_b32 s63, v237, 32
	s_add_u32 s6, s62, s6
	s_addc_u32 s7, s63, s7
	v_ashrrev_i32_e32 v19, 31, v18
	s_nop 15
	s_nop 15
	s_nop 15
	v_lshl_add_u64 v[2:3], v[18:19], 2, s[6:7]
	global_load_dwordx4 v[14:17], v[2:3], off
	global_load_dwordx4 v[6:9], v[2:3], off offset:16
	v_add_co_u32_e32 v4, vcc, s44, v2
	s_lshl_b32 s5, s26, 8
	s_nop 0
	v_addc_co_u32_e32 v5, vcc, 0, v3, vcc
	global_load_dwordx4 v[10:13], v[4:5], off
	v_lshl_add_u64 v[2:3], v[2:3], 0, s[14:15]
	global_load_dwordx4 v[2:5], v[2:3], off offset:16
	v_readlane_b32 s61, v237, 30
	v_readlane_b32 s64, v237, 33
	v_readlane_b32 s65, v237, 34
	v_readlane_b32 s66, v237, 35
	v_readlane_b32 s67, v237, 36
	v_readlane_b32 s68, v237, 37
	v_readlane_b32 s69, v237, 38
	v_readlane_b32 s70, v237, 39
	v_readlane_b32 s71, v237, 40
	v_readlane_b32 s72, v237, 41
	v_readlane_b32 s73, v237, 42
	v_readlane_b32 s74, v237, 43
	v_readlane_b32 s75, v237, 44
	v_readlane_b32 s60, v238, 13
	v_readlane_b32 s74, v238, 27
	v_readlane_b32 s75, v238, 28
	s_andn2_b64 vcc, exec, s[0:1]
	s_mov_b64 s[0:1], -1
	v_readlane_b32 s61, v238, 14
	v_readlane_b32 s62, v238, 15
	v_readlane_b32 s63, v238, 16
	v_readlane_b32 s64, v238, 17
	v_readlane_b32 s65, v238, 18
	v_readlane_b32 s66, v238, 19
	v_readlane_b32 s67, v238, 20
	v_readlane_b32 s68, v238, 21
	v_readlane_b32 s69, v238, 22
	v_readlane_b32 s70, v238, 23
	v_readlane_b32 s71, v238, 24
	v_readlane_b32 s72, v238, 25
	v_readlane_b32 s73, v238, 26
	s_waitcnt vmcnt(0)
	v_fmamk_f32 v20, v158, 0x39800000, v14
	v_min_f32_e32 v20, 0x40e00000, v20
	v_mul_f32_e32 v28, 0xc01d265f, v20
	v_fmamk_f32 v21, v159, 0x39800000, v15
	v_min_f32_e32 v21, 0x40e00000, v21
	v_exp_f32_e32 v28, v28
	v_mul_f32_e32 v30, 0xc01d265f, v21
	v_exp_f32_e32 v30, v30
	v_add_f32_e32 v28, 1.0, v28
	v_rcp_f32_e32 v28, v28
	v_fmamk_f32 v27, v154, 0x39800000, v10
	v_fmamk_f32 v26, v148, 0x39800000, v8
	v_med3_f32 v27, v27, s50, v190
	v_add_f32_e32 v30, 1.0, v30
	v_min_f32_e32 v26, 0x40e00000, v26
	v_fma_f32 v27, v27, 4.0, 4.0
	v_rcp_f32_e32 v30, v30
	v_fmamk_f32 v29, v155, 0x39800000, v11
	v_mul_f32_e32 v20, v20, v28
	v_med3_f32 v29, v29, s50, v190
	v_mul_f32_e32 v27, v27, v20
	v_mul_f32_e32 v20, 0xc01d265f, v26
	v_fmamk_f32 v22, v160, 0x39800000, v16
	v_fma_f32 v29, v29, 4.0, 4.0
	v_exp_f32_e32 v20, v20
	v_fmamk_f32 v23, v161, 0x39800000, v17
	v_fmamk_f32 v24, v146, 0x39800000, v6
	v_fmamk_f32 v25, v147, 0x39800000, v7
	v_min_f32_e32 v22, 0x40e00000, v22
	v_mul_f32_e32 v21, v21, v30
	v_min_f32_e32 v23, 0x40e00000, v23
	v_min_f32_e32 v24, 0x40e00000, v24
	v_min_f32_e32 v25, 0x40e00000, v25
	v_mul_f32_e32 v32, 0xc01d265f, v22
	v_mul_f32_e32 v21, v29, v21
	v_fmamk_f32 v29, v149, 0x39800000, v9
	v_mul_f32_e32 v146, 0xc01d265f, v23
	v_fmamk_f32 v147, v150, 0x39800000, v2
	v_mul_f32_e32 v148, 0xc01d265f, v24
	v_fmamk_f32 v150, v151, 0x39800000, v3
	v_mul_f32_e32 v151, 0xc01d265f, v25
	v_min_f32_e32 v29, 0x40e00000, v29
	v_exp_f32_e32 v32, v32
	v_add_f32_e32 v20, 1.0, v20
	v_mul_f32_e32 v30, 0xc01d265f, v29
	v_exp_f32_e32 v146, v146
	v_exp_f32_e32 v148, v148
	v_exp_f32_e32 v151, v151
	v_rcp_f32_e32 v20, v20
	v_fmamk_f32 v152, v152, 0x39800000, v4
	v_exp_f32_e32 v30, v30
	v_med3_f32 v28, v152, s50, v190
	v_add_f32_e32 v32, 1.0, v32
	v_fma_f32 v28, v28, 4.0, 4.0
	v_add_f32_e32 v146, 1.0, v146
	v_add_f32_e32 v148, 1.0, v148
	v_add_f32_e32 v151, 1.0, v151
	v_rcp_f32_e32 v32, v32
	v_mul_f32_e32 v20, v26, v20
	v_fmamk_f32 v31, v156, 0x39800000, v12
	v_rcp_f32_e32 v146, v146
	v_rcp_f32_e32 v148, v148
	v_rcp_f32_e32 v151, v151
	v_mul_f32_e32 v26, v28, v20
	v_add_f32_e32 v28, 1.0, v30
	v_fmamk_f32 v33, v157, 0x39800000, v13
	v_med3_f32 v31, v31, s50, v190
	v_rcp_f32_e32 v28, v28
	v_med3_f32 v33, v33, s50, v190
	v_med3_f32 v147, v147, s50, v190
	v_med3_f32 v150, v150, s50, v190
	v_fma_f32 v31, v31, 4.0, 4.0
	v_fma_f32 v33, v33, 4.0, 4.0
	v_fma_f32 v147, v147, 4.0, 4.0
	v_fma_f32 v150, v150, 4.0, 4.0
	v_mul_f32_e32 v22, v22, v32
	v_mul_f32_e32 v23, v23, v146
	v_mul_f32_e32 v24, v24, v148
	v_mul_f32_e32 v25, v25, v151
	v_mul_f32_e32 v22, v31, v22
	v_mul_f32_e32 v23, v33, v23
	v_mul_f32_e32 v24, v147, v24
	v_mul_f32_e32 v25, v150, v25
	v_fmamk_f32 v20, v153, 0x39800000, v5
	v_mul_f32_e32 v28, v29, v28
	v_mov_b32_e32 v29, v22
	v_med3_f32 v20, v20, s50, v190
	v_mov_b32_e32 v30, v23
	v_cvt_pk_fp8_f32 v22, v27, v21
	v_mov_b32_e32 v21, v24
	v_mov_b32_e32 v24, v25
	v_fma_f32 v20, v20, 4.0, 4.0
	v_cvt_pk_fp8_f32 v23, v21, v24
	v_mul_f32_e32 v28, v20, v28
	v_add_u32_e32 v20, s5, v1
	v_mov_b32_e32 v21, v26
	v_mov_b32_e32 v24, v28
	v_cvt_pk_fp8_f32 v22, v29, v30 op_sel:[0,0,1]
	v_cvt_pk_fp8_f32 v23, v21, v24 op_sel:[0,0,1]
	v_ashrrev_i32_e32 v21, 31, v20
	v_lshlrev_b64 v[24:25], 11, v[20:21]
	v_lshl_add_u64 v[24:25], s[74:75], 0, v[24:25]
	v_fmamk_f32 v21, v138, 0x39800000, v14
	v_lshl_add_u64 v[24:25], v[24:25], 0, v[18:19]
	v_min_f32_e32 v21, 0x40e00000, v21
	global_store_dwordx2 v[24:25], v[22:23], off
	v_mul_f32_e32 v23, 0xc01d265f, v21
	v_exp_f32_e32 v23, v23
	v_fmamk_f32 v24, v139, 0x39800000, v15
	v_min_f32_e32 v24, 0x40e00000, v24
	v_mul_f32_e32 v25, 0xc01d265f, v24
	v_add_f32_e32 v23, 1.0, v23
	v_rcp_f32_e32 v23, v23
	v_exp_f32_e32 v25, v25
	v_fmamk_f32 v22, v142, 0x39800000, v10
	v_med3_f32 v22, v22, s50, v190
	v_fma_f32 v22, v22, 4.0, 4.0
	v_mul_f32_e32 v21, v21, v23
	v_add_f32_e32 v23, 1.0, v25
	v_rcp_f32_e32 v23, v23
	v_mul_f32_e32 v21, v22, v21
	v_fmamk_f32 v22, v143, 0x39800000, v11
	v_med3_f32 v22, v22, s50, v190
	v_fma_f32 v22, v22, 4.0, 4.0
	v_mul_f32_e32 v23, v24, v23
	v_mul_f32_e32 v23, v22, v23
	v_fmamk_f32 v22, v140, 0x39800000, v16
	v_min_f32_e32 v22, 0x40e00000, v22
	v_mul_f32_e32 v25, 0xc01d265f, v22
	v_exp_f32_e32 v25, v25
	v_fmamk_f32 v26, v141, 0x39800000, v17
	v_min_f32_e32 v26, 0x40e00000, v26
	v_mul_f32_e32 v27, 0xc01d265f, v26
	v_add_f32_e32 v25, 1.0, v25
	v_rcp_f32_e32 v25, v25
	v_exp_f32_e32 v27, v27
	v_fmamk_f32 v24, v144, 0x39800000, v12
	v_med3_f32 v24, v24, s50, v190
	v_fma_f32 v24, v24, 4.0, 4.0
	v_mul_f32_e32 v22, v22, v25
	v_add_f32_e32 v25, 1.0, v27
	v_rcp_f32_e32 v25, v25
	v_mul_f32_e32 v24, v24, v22
	v_fmamk_f32 v22, v145, 0x39800000, v13
	v_med3_f32 v22, v22, s50, v190
	v_fma_f32 v22, v22, 4.0, 4.0
	v_mul_f32_e32 v25, v26, v25
	v_mul_f32_e32 v25, v22, v25
	v_fmamk_f32 v22, v130, 0x39800000, v6
	v_min_f32_e32 v22, 0x40e00000, v22
	v_mul_f32_e32 v27, 0xc01d265f, v22
	v_exp_f32_e32 v27, v27
	v_fmamk_f32 v28, v131, 0x39800000, v7
	v_min_f32_e32 v28, 0x40e00000, v28
	v_mul_f32_e32 v29, 0xc01d265f, v28
	v_add_f32_e32 v27, 1.0, v27
	v_rcp_f32_e32 v27, v27
	v_exp_f32_e32 v29, v29
	v_fmamk_f32 v26, v134, 0x39800000, v2
	v_med3_f32 v26, v26, s50, v190
	v_fma_f32 v26, v26, 4.0, 4.0
	v_mul_f32_e32 v22, v22, v27
	v_add_f32_e32 v27, 1.0, v29
	v_rcp_f32_e32 v27, v27
	v_mul_f32_e32 v26, v26, v22
	v_fmamk_f32 v22, v135, 0x39800000, v3
	v_med3_f32 v22, v22, s50, v190
	v_fma_f32 v22, v22, 4.0, 4.0
	v_mul_f32_e32 v27, v28, v27
	v_mul_f32_e32 v27, v22, v27
	v_fmamk_f32 v22, v132, 0x39800000, v8
	v_min_f32_e32 v22, 0x40e00000, v22
	v_mul_f32_e32 v29, 0xc01d265f, v22
	v_exp_f32_e32 v29, v29
	v_fmamk_f32 v30, v133, 0x39800000, v9
	v_min_f32_e32 v30, 0x40e00000, v30
	v_mul_f32_e32 v31, 0xc01d265f, v30
	v_add_f32_e32 v29, 1.0, v29
	v_rcp_f32_e32 v29, v29
	v_exp_f32_e32 v31, v31
	v_fmamk_f32 v28, v136, 0x39800000, v4
	v_med3_f32 v28, v28, s50, v190
	v_mul_f32_e32 v22, v22, v29
	v_add_f32_e32 v29, 1.0, v31
	v_rcp_f32_e32 v29, v29
	v_fma_f32 v28, v28, 4.0, 4.0
	v_mul_f32_e32 v28, v28, v22
	v_fmamk_f32 v22, v137, 0x39800000, v5
	v_mul_f32_e32 v29, v30, v29
	v_mov_b32_e32 v30, v24
	v_med3_f32 v22, v22, s50, v190
	v_mov_b32_e32 v31, v25
	v_cvt_pk_fp8_f32 v24, v21, v23
	v_mov_b32_e32 v21, v26
	v_mov_b32_e32 v23, v27
	v_fma_f32 v22, v22, 4.0, 4.0
	v_cvt_pk_fp8_f32 v25, v21, v23
	v_mul_f32_e32 v29, v22, v29
	v_add_u32_e32 v22, s5, v185
	v_mov_b32_e32 v21, v28
	v_mov_b32_e32 v23, v29
	v_cvt_pk_fp8_f32 v24, v30, v31 op_sel:[0,0,1]
	v_cvt_pk_fp8_f32 v25, v21, v23 op_sel:[0,0,1]
	v_ashrrev_i32_e32 v23, 31, v22
	v_lshlrev_b64 v[22:23], 11, v[22:23]
	v_lshl_add_u64 v[22:23], s[74:75], 0, v[22:23]
	v_fmamk_f32 v21, v122, 0x39800000, v14
	v_lshl_add_u64 v[22:23], v[22:23], 0, v[18:19]
	v_min_f32_e32 v21, 0x40e00000, v21
	global_store_dwordx2 v[22:23], v[24:25], off
	v_mul_f32_e32 v23, 0xc01d265f, v21
	v_exp_f32_e32 v23, v23
	v_fmamk_f32 v24, v123, 0x39800000, v15
	v_min_f32_e32 v24, 0x40e00000, v24
	v_mul_f32_e32 v25, 0xc01d265f, v24
	v_add_f32_e32 v23, 1.0, v23
	v_rcp_f32_e32 v23, v23
	v_exp_f32_e32 v25, v25
	v_fmamk_f32 v22, v126, 0x39800000, v10
	v_med3_f32 v22, v22, s50, v190
	v_fma_f32 v22, v22, 4.0, 4.0
	v_mul_f32_e32 v21, v21, v23
	v_add_f32_e32 v23, 1.0, v25
	v_rcp_f32_e32 v23, v23
	v_mul_f32_e32 v21, v22, v21
	v_fmamk_f32 v22, v127, 0x39800000, v11
	v_med3_f32 v22, v22, s50, v190
	v_fma_f32 v22, v22, 4.0, 4.0
	v_mul_f32_e32 v23, v24, v23
	v_mul_f32_e32 v23, v22, v23
	v_fmamk_f32 v22, v124, 0x39800000, v16
	v_min_f32_e32 v22, 0x40e00000, v22
	v_mul_f32_e32 v25, 0xc01d265f, v22
	v_exp_f32_e32 v25, v25
	v_fmamk_f32 v26, v125, 0x39800000, v17
	v_min_f32_e32 v26, 0x40e00000, v26
	v_mul_f32_e32 v27, 0xc01d265f, v26
	v_add_f32_e32 v25, 1.0, v25
	v_rcp_f32_e32 v25, v25
	v_exp_f32_e32 v27, v27
	v_fmamk_f32 v24, v128, 0x39800000, v12
	v_med3_f32 v24, v24, s50, v190
	v_fma_f32 v24, v24, 4.0, 4.0
	v_mul_f32_e32 v22, v22, v25
	v_add_f32_e32 v25, 1.0, v27
	v_rcp_f32_e32 v25, v25
	v_mul_f32_e32 v24, v24, v22
	v_fmamk_f32 v22, v129, 0x39800000, v13
	v_med3_f32 v22, v22, s50, v190
	v_fma_f32 v22, v22, 4.0, 4.0
	v_mul_f32_e32 v25, v26, v25
	v_mul_f32_e32 v25, v22, v25
	v_fmamk_f32 v22, v114, 0x39800000, v6
	v_min_f32_e32 v22, 0x40e00000, v22
	v_mul_f32_e32 v27, 0xc01d265f, v22
	v_exp_f32_e32 v27, v27
	v_fmamk_f32 v28, v115, 0x39800000, v7
	v_min_f32_e32 v28, 0x40e00000, v28
	v_mul_f32_e32 v29, 0xc01d265f, v28
	v_add_f32_e32 v27, 1.0, v27
	v_rcp_f32_e32 v27, v27
	v_exp_f32_e32 v29, v29
	v_fmamk_f32 v26, v118, 0x39800000, v2
	v_med3_f32 v26, v26, s50, v190
	v_fma_f32 v26, v26, 4.0, 4.0
	v_mul_f32_e32 v22, v22, v27
	v_add_f32_e32 v27, 1.0, v29
	v_rcp_f32_e32 v27, v27
	v_mul_f32_e32 v26, v26, v22
	v_fmamk_f32 v22, v119, 0x39800000, v3
	v_med3_f32 v22, v22, s50, v190
	v_fma_f32 v22, v22, 4.0, 4.0
	v_mul_f32_e32 v27, v28, v27
	v_mul_f32_e32 v27, v22, v27
	v_fmamk_f32 v22, v116, 0x39800000, v8
	v_min_f32_e32 v22, 0x40e00000, v22
	v_mul_f32_e32 v29, 0xc01d265f, v22
	v_exp_f32_e32 v29, v29
	v_fmamk_f32 v30, v117, 0x39800000, v9
	v_min_f32_e32 v30, 0x40e00000, v30
	v_mul_f32_e32 v31, 0xc01d265f, v30
	v_add_f32_e32 v29, 1.0, v29
	v_rcp_f32_e32 v29, v29
	v_exp_f32_e32 v31, v31
	v_fmamk_f32 v28, v120, 0x39800000, v4
	v_med3_f32 v28, v28, s50, v190
	v_mul_f32_e32 v22, v22, v29
	v_add_f32_e32 v29, 1.0, v31
	v_rcp_f32_e32 v29, v29
	v_fma_f32 v28, v28, 4.0, 4.0
	v_mul_f32_e32 v28, v28, v22
	v_fmamk_f32 v22, v121, 0x39800000, v5
	v_mul_f32_e32 v29, v30, v29
	v_mov_b32_e32 v30, v24
	v_med3_f32 v22, v22, s50, v190
	v_mov_b32_e32 v31, v25
	v_cvt_pk_fp8_f32 v24, v21, v23
	v_mov_b32_e32 v21, v26
	v_mov_b32_e32 v23, v27
	v_fma_f32 v22, v22, 4.0, 4.0
	v_cvt_pk_fp8_f32 v25, v21, v23
	v_mul_f32_e32 v29, v22, v29
	v_add_u32_e32 v22, s5, v186
	v_mov_b32_e32 v21, v28
	v_mov_b32_e32 v23, v29
	v_cvt_pk_fp8_f32 v24, v30, v31 op_sel:[0,0,1]
	v_cvt_pk_fp8_f32 v25, v21, v23 op_sel:[0,0,1]
	v_ashrrev_i32_e32 v23, 31, v22
	v_lshlrev_b64 v[22:23], 11, v[22:23]
	v_lshl_add_u64 v[22:23], s[74:75], 0, v[22:23]
	v_fmamk_f32 v21, v106, 0x39800000, v14
	v_lshl_add_u64 v[22:23], v[22:23], 0, v[18:19]
	v_min_f32_e32 v21, 0x40e00000, v21
	global_store_dwordx2 v[22:23], v[24:25], off
	v_mul_f32_e32 v23, 0xc01d265f, v21
	v_exp_f32_e32 v23, v23
	v_fmamk_f32 v24, v107, 0x39800000, v15
	v_min_f32_e32 v24, 0x40e00000, v24
	v_mul_f32_e32 v25, 0xc01d265f, v24
	v_add_f32_e32 v23, 1.0, v23
	v_rcp_f32_e32 v23, v23
	v_exp_f32_e32 v25, v25
	v_fmamk_f32 v22, v110, 0x39800000, v10
	v_med3_f32 v22, v22, s50, v190
	v_fma_f32 v22, v22, 4.0, 4.0
	v_mul_f32_e32 v21, v21, v23
	v_add_f32_e32 v23, 1.0, v25
	v_rcp_f32_e32 v23, v23
	v_mul_f32_e32 v21, v22, v21
	v_fmamk_f32 v22, v111, 0x39800000, v11
	v_med3_f32 v22, v22, s50, v190
	v_fma_f32 v22, v22, 4.0, 4.0
	v_mul_f32_e32 v23, v24, v23
	v_mul_f32_e32 v23, v22, v23
	v_fmamk_f32 v22, v108, 0x39800000, v16
	v_min_f32_e32 v22, 0x40e00000, v22
	v_mul_f32_e32 v25, 0xc01d265f, v22
	v_exp_f32_e32 v25, v25
	v_fmamk_f32 v26, v109, 0x39800000, v17
	v_min_f32_e32 v26, 0x40e00000, v26
	v_mul_f32_e32 v27, 0xc01d265f, v26
	v_add_f32_e32 v25, 1.0, v25
	v_rcp_f32_e32 v25, v25
	v_exp_f32_e32 v27, v27
	v_fmamk_f32 v24, v112, 0x39800000, v12
	v_med3_f32 v24, v24, s50, v190
	v_fma_f32 v24, v24, 4.0, 4.0
	v_mul_f32_e32 v22, v22, v25
	v_add_f32_e32 v25, 1.0, v27
	v_rcp_f32_e32 v25, v25
	v_mul_f32_e32 v24, v24, v22
	v_fmamk_f32 v22, v113, 0x39800000, v13
	v_med3_f32 v22, v22, s50, v190
	v_fma_f32 v22, v22, 4.0, 4.0
	v_mul_f32_e32 v25, v26, v25
	v_mul_f32_e32 v25, v22, v25
	v_fmamk_f32 v22, v98, 0x39800000, v6
	v_min_f32_e32 v22, 0x40e00000, v22
	v_mul_f32_e32 v27, 0xc01d265f, v22
	v_exp_f32_e32 v27, v27
	v_fmamk_f32 v28, v99, 0x39800000, v7
	v_min_f32_e32 v28, 0x40e00000, v28
	v_mul_f32_e32 v29, 0xc01d265f, v28
	v_add_f32_e32 v27, 1.0, v27
	v_rcp_f32_e32 v27, v27
	v_exp_f32_e32 v29, v29
	v_fmamk_f32 v26, v102, 0x39800000, v2
	v_med3_f32 v26, v26, s50, v190
	v_fma_f32 v26, v26, 4.0, 4.0
	v_mul_f32_e32 v22, v22, v27
	v_add_f32_e32 v27, 1.0, v29
	v_rcp_f32_e32 v27, v27
	v_mul_f32_e32 v26, v26, v22
	v_fmamk_f32 v22, v103, 0x39800000, v3
	v_med3_f32 v22, v22, s50, v190
	v_fma_f32 v22, v22, 4.0, 4.0
	v_mul_f32_e32 v27, v28, v27
	v_mul_f32_e32 v27, v22, v27
	v_fmamk_f32 v22, v100, 0x39800000, v8
	v_min_f32_e32 v22, 0x40e00000, v22
	v_mul_f32_e32 v29, 0xc01d265f, v22
	v_exp_f32_e32 v29, v29
	v_fmamk_f32 v30, v101, 0x39800000, v9
	v_min_f32_e32 v30, 0x40e00000, v30
	v_mul_f32_e32 v31, 0xc01d265f, v30
	v_add_f32_e32 v29, 1.0, v29
	v_rcp_f32_e32 v29, v29
	v_exp_f32_e32 v31, v31
	v_fmamk_f32 v28, v104, 0x39800000, v4
	v_med3_f32 v28, v28, s50, v190
	v_mul_f32_e32 v22, v22, v29
	v_add_f32_e32 v29, 1.0, v31
	v_rcp_f32_e32 v29, v29
	v_fma_f32 v28, v28, 4.0, 4.0
	v_mul_f32_e32 v28, v28, v22
	v_fmamk_f32 v22, v105, 0x39800000, v5
	v_mul_f32_e32 v29, v30, v29
	v_mov_b32_e32 v30, v24
	v_med3_f32 v22, v22, s50, v190
	v_mov_b32_e32 v31, v25
	v_cvt_pk_fp8_f32 v24, v21, v23
	v_mov_b32_e32 v21, v26
	v_mov_b32_e32 v23, v27
	v_fma_f32 v22, v22, 4.0, 4.0
	v_cvt_pk_fp8_f32 v25, v21, v23
	v_mul_f32_e32 v29, v22, v29
	v_add_u32_e32 v22, s5, v187
	v_mov_b32_e32 v21, v28
	v_mov_b32_e32 v23, v29
	v_cvt_pk_fp8_f32 v24, v30, v31 op_sel:[0,0,1]
	v_cvt_pk_fp8_f32 v25, v21, v23 op_sel:[0,0,1]
	v_ashrrev_i32_e32 v23, 31, v22
	v_lshlrev_b64 v[22:23], 11, v[22:23]
	v_lshl_add_u64 v[22:23], s[74:75], 0, v[22:23]
	v_fmamk_f32 v21, v90, 0x39800000, v14
	v_lshl_add_u64 v[22:23], v[22:23], 0, v[18:19]
	v_min_f32_e32 v21, 0x40e00000, v21
	global_store_dwordx2 v[22:23], v[24:25], off
	v_mul_f32_e32 v23, 0xc01d265f, v21
	v_exp_f32_e32 v23, v23
	v_fmamk_f32 v24, v91, 0x39800000, v15
	v_min_f32_e32 v24, 0x40e00000, v24
	v_mul_f32_e32 v25, 0xc01d265f, v24
	v_add_f32_e32 v23, 1.0, v23
	v_rcp_f32_e32 v23, v23
	v_exp_f32_e32 v25, v25
	v_fmamk_f32 v22, v94, 0x39800000, v10
	v_med3_f32 v22, v22, s50, v190
	v_fma_f32 v22, v22, 4.0, 4.0
	v_mul_f32_e32 v21, v21, v23
	v_add_f32_e32 v23, 1.0, v25
	v_rcp_f32_e32 v23, v23
	v_mul_f32_e32 v21, v22, v21
	v_fmamk_f32 v22, v95, 0x39800000, v11
	v_med3_f32 v22, v22, s50, v190
	v_fma_f32 v22, v22, 4.0, 4.0
	v_mul_f32_e32 v23, v24, v23
	v_mul_f32_e32 v23, v22, v23
	v_fmamk_f32 v22, v92, 0x39800000, v16
	v_min_f32_e32 v22, 0x40e00000, v22
	v_mul_f32_e32 v25, 0xc01d265f, v22
	v_exp_f32_e32 v25, v25
	v_fmamk_f32 v26, v93, 0x39800000, v17
	v_min_f32_e32 v26, 0x40e00000, v26
	v_mul_f32_e32 v27, 0xc01d265f, v26
	v_add_f32_e32 v25, 1.0, v25
	v_rcp_f32_e32 v25, v25
	v_exp_f32_e32 v27, v27
	v_fmamk_f32 v24, v96, 0x39800000, v12
	v_med3_f32 v24, v24, s50, v190
	v_fma_f32 v24, v24, 4.0, 4.0
	v_mul_f32_e32 v22, v22, v25
	v_add_f32_e32 v25, 1.0, v27
	v_rcp_f32_e32 v25, v25
	v_mul_f32_e32 v24, v24, v22
	v_fmamk_f32 v22, v97, 0x39800000, v13
	v_med3_f32 v22, v22, s50, v190
	v_fma_f32 v22, v22, 4.0, 4.0
	v_mul_f32_e32 v25, v26, v25
	v_mul_f32_e32 v25, v22, v25
	v_fmamk_f32 v22, v82, 0x39800000, v6
	v_min_f32_e32 v22, 0x40e00000, v22
	v_mul_f32_e32 v27, 0xc01d265f, v22
	v_exp_f32_e32 v27, v27
	v_fmamk_f32 v28, v83, 0x39800000, v7
	v_min_f32_e32 v28, 0x40e00000, v28
	v_mul_f32_e32 v29, 0xc01d265f, v28
	v_add_f32_e32 v27, 1.0, v27
	v_rcp_f32_e32 v27, v27
	v_exp_f32_e32 v29, v29
	v_fmamk_f32 v26, v86, 0x39800000, v2
	v_med3_f32 v26, v26, s50, v190
	v_fma_f32 v26, v26, 4.0, 4.0
	v_mul_f32_e32 v22, v22, v27
	v_add_f32_e32 v27, 1.0, v29
	v_rcp_f32_e32 v27, v27
	v_mul_f32_e32 v26, v26, v22
	v_fmamk_f32 v22, v87, 0x39800000, v3
	v_med3_f32 v22, v22, s50, v190
	v_fma_f32 v22, v22, 4.0, 4.0
	v_mul_f32_e32 v27, v28, v27
	v_mul_f32_e32 v27, v22, v27
	v_fmamk_f32 v22, v84, 0x39800000, v8
	v_min_f32_e32 v22, 0x40e00000, v22
	v_mul_f32_e32 v29, 0xc01d265f, v22
	v_exp_f32_e32 v29, v29
	v_fmamk_f32 v30, v85, 0x39800000, v9
	v_min_f32_e32 v30, 0x40e00000, v30
	v_mul_f32_e32 v31, 0xc01d265f, v30
	v_add_f32_e32 v29, 1.0, v29
	v_rcp_f32_e32 v29, v29
	v_exp_f32_e32 v31, v31
	v_fmamk_f32 v28, v88, 0x39800000, v4
	v_med3_f32 v28, v28, s50, v190
	v_mul_f32_e32 v22, v22, v29
	v_add_f32_e32 v29, 1.0, v31
	v_rcp_f32_e32 v29, v29
	v_fma_f32 v28, v28, 4.0, 4.0
	v_mul_f32_e32 v28, v28, v22
	v_fmamk_f32 v22, v89, 0x39800000, v5
	v_mul_f32_e32 v29, v30, v29
	v_mov_b32_e32 v30, v24
	v_med3_f32 v22, v22, s50, v190
	v_mov_b32_e32 v31, v25
	v_cvt_pk_fp8_f32 v24, v21, v23
	v_mov_b32_e32 v21, v26
	v_mov_b32_e32 v23, v27
	v_fma_f32 v22, v22, 4.0, 4.0
	v_cvt_pk_fp8_f32 v25, v21, v23
	v_mul_f32_e32 v29, v22, v29
	v_add_u32_e32 v22, 0x80, v20
	v_mov_b32_e32 v21, v28
	v_mov_b32_e32 v23, v29
	v_cvt_pk_fp8_f32 v24, v30, v31 op_sel:[0,0,1]
	v_cvt_pk_fp8_f32 v25, v21, v23 op_sel:[0,0,1]
	v_ashrrev_i32_e32 v23, 31, v22
	v_lshlrev_b64 v[22:23], 11, v[22:23]
	v_lshl_add_u64 v[22:23], s[74:75], 0, v[22:23]
	v_fmamk_f32 v21, v74, 0x39800000, v14
	v_lshl_add_u64 v[22:23], v[22:23], 0, v[18:19]
	v_min_f32_e32 v21, 0x40e00000, v21
	global_store_dwordx2 v[22:23], v[24:25], off
	v_mul_f32_e32 v23, 0xc01d265f, v21
	v_exp_f32_e32 v23, v23
	v_fmamk_f32 v24, v75, 0x39800000, v15
	v_min_f32_e32 v24, 0x40e00000, v24
	v_mul_f32_e32 v25, 0xc01d265f, v24
	v_add_f32_e32 v23, 1.0, v23
	v_rcp_f32_e32 v23, v23
	v_exp_f32_e32 v25, v25
	v_fmamk_f32 v22, v78, 0x39800000, v10
	v_med3_f32 v22, v22, s50, v190
	v_fma_f32 v22, v22, 4.0, 4.0
	v_mul_f32_e32 v21, v21, v23
	v_add_f32_e32 v23, 1.0, v25
	v_rcp_f32_e32 v23, v23
	v_mul_f32_e32 v21, v22, v21
	v_fmamk_f32 v22, v79, 0x39800000, v11
	v_med3_f32 v22, v22, s50, v190
	v_fma_f32 v22, v22, 4.0, 4.0
	v_mul_f32_e32 v23, v24, v23
	v_mul_f32_e32 v23, v22, v23
	v_fmamk_f32 v22, v76, 0x39800000, v16
	v_min_f32_e32 v22, 0x40e00000, v22
	v_mul_f32_e32 v25, 0xc01d265f, v22
	v_exp_f32_e32 v25, v25
	v_fmamk_f32 v26, v77, 0x39800000, v17
	v_min_f32_e32 v26, 0x40e00000, v26
	v_mul_f32_e32 v27, 0xc01d265f, v26
	v_add_f32_e32 v25, 1.0, v25
	v_rcp_f32_e32 v25, v25
	v_exp_f32_e32 v27, v27
	v_fmamk_f32 v24, v80, 0x39800000, v12
	v_med3_f32 v24, v24, s50, v190
	v_fma_f32 v24, v24, 4.0, 4.0
	v_mul_f32_e32 v22, v22, v25
	v_add_f32_e32 v25, 1.0, v27
	v_rcp_f32_e32 v25, v25
	v_mul_f32_e32 v24, v24, v22
	v_fmamk_f32 v22, v81, 0x39800000, v13
	v_med3_f32 v22, v22, s50, v190
	v_fma_f32 v22, v22, 4.0, 4.0
	v_mul_f32_e32 v25, v26, v25
	v_mul_f32_e32 v25, v22, v25
	v_fmamk_f32 v22, v66, 0x39800000, v6
	v_min_f32_e32 v22, 0x40e00000, v22
	v_mul_f32_e32 v27, 0xc01d265f, v22
	v_exp_f32_e32 v27, v27
	v_fmamk_f32 v28, v67, 0x39800000, v7
	v_min_f32_e32 v28, 0x40e00000, v28
	v_mul_f32_e32 v29, 0xc01d265f, v28
	v_add_f32_e32 v27, 1.0, v27
	v_rcp_f32_e32 v27, v27
	v_exp_f32_e32 v29, v29
	v_fmamk_f32 v26, v70, 0x39800000, v2
	v_med3_f32 v26, v26, s50, v190
	v_fma_f32 v26, v26, 4.0, 4.0
	v_mul_f32_e32 v22, v22, v27
	v_add_f32_e32 v27, 1.0, v29
	v_rcp_f32_e32 v27, v27
	v_mul_f32_e32 v26, v26, v22
	v_fmamk_f32 v22, v71, 0x39800000, v3
	v_med3_f32 v22, v22, s50, v190
	v_fma_f32 v22, v22, 4.0, 4.0
	v_mul_f32_e32 v27, v28, v27
	v_mul_f32_e32 v27, v22, v27
	v_fmamk_f32 v22, v68, 0x39800000, v8
	v_min_f32_e32 v22, 0x40e00000, v22
	v_mul_f32_e32 v29, 0xc01d265f, v22
	v_exp_f32_e32 v29, v29
	v_fmamk_f32 v30, v69, 0x39800000, v9
	v_min_f32_e32 v30, 0x40e00000, v30
	v_mul_f32_e32 v31, 0xc01d265f, v30
	v_add_f32_e32 v29, 1.0, v29
	v_rcp_f32_e32 v29, v29
	v_exp_f32_e32 v31, v31
	v_fmamk_f32 v28, v72, 0x39800000, v4
	v_med3_f32 v28, v28, s50, v190
	v_mul_f32_e32 v22, v22, v29
	v_add_f32_e32 v29, 1.0, v31
	v_rcp_f32_e32 v29, v29
	v_fma_f32 v28, v28, 4.0, 4.0
	v_mul_f32_e32 v28, v28, v22
	v_fmamk_f32 v22, v73, 0x39800000, v5
	v_mul_f32_e32 v29, v30, v29
	v_mov_b32_e32 v30, v24
	v_med3_f32 v22, v22, s50, v190
	v_mov_b32_e32 v31, v25
	v_cvt_pk_fp8_f32 v24, v21, v23
	v_mov_b32_e32 v21, v26
	v_mov_b32_e32 v23, v27
	v_fma_f32 v22, v22, 4.0, 4.0
	v_cvt_pk_fp8_f32 v25, v21, v23
	v_mul_f32_e32 v29, v22, v29
	v_add_u32_e32 v22, 0x90, v20
	v_mov_b32_e32 v21, v28
	v_mov_b32_e32 v23, v29
	v_cvt_pk_fp8_f32 v24, v30, v31 op_sel:[0,0,1]
	v_cvt_pk_fp8_f32 v25, v21, v23 op_sel:[0,0,1]
	v_ashrrev_i32_e32 v23, 31, v22
	v_lshlrev_b64 v[22:23], 11, v[22:23]
	v_lshl_add_u64 v[22:23], s[74:75], 0, v[22:23]
	v_fmamk_f32 v21, v58, 0x39800000, v14
	v_lshl_add_u64 v[22:23], v[22:23], 0, v[18:19]
	v_min_f32_e32 v21, 0x40e00000, v21
	global_store_dwordx2 v[22:23], v[24:25], off
	v_mul_f32_e32 v23, 0xc01d265f, v21
	v_exp_f32_e32 v23, v23
	v_fmamk_f32 v24, v59, 0x39800000, v15
	v_min_f32_e32 v24, 0x40e00000, v24
	v_mul_f32_e32 v25, 0xc01d265f, v24
	v_add_f32_e32 v23, 1.0, v23
	v_rcp_f32_e32 v23, v23
	v_exp_f32_e32 v25, v25
	v_fmamk_f32 v22, v62, 0x39800000, v10
	v_med3_f32 v22, v22, s50, v190
	v_fma_f32 v22, v22, 4.0, 4.0
	v_mul_f32_e32 v21, v21, v23
	v_add_f32_e32 v23, 1.0, v25
	v_rcp_f32_e32 v23, v23
	v_mul_f32_e32 v21, v22, v21
	v_fmamk_f32 v22, v63, 0x39800000, v11
	v_med3_f32 v22, v22, s50, v190
	v_fma_f32 v22, v22, 4.0, 4.0
	v_mul_f32_e32 v23, v24, v23
	v_mul_f32_e32 v23, v22, v23
	v_fmamk_f32 v22, v60, 0x39800000, v16
	v_min_f32_e32 v22, 0x40e00000, v22
	v_mul_f32_e32 v25, 0xc01d265f, v22
	v_exp_f32_e32 v25, v25
	v_fmamk_f32 v26, v61, 0x39800000, v17
	v_min_f32_e32 v26, 0x40e00000, v26
	v_mul_f32_e32 v27, 0xc01d265f, v26
	v_add_f32_e32 v25, 1.0, v25
	v_rcp_f32_e32 v25, v25
	v_exp_f32_e32 v27, v27
	v_fmamk_f32 v24, v64, 0x39800000, v12
	v_med3_f32 v24, v24, s50, v190
	v_fma_f32 v24, v24, 4.0, 4.0
	v_mul_f32_e32 v22, v22, v25
	v_add_f32_e32 v25, 1.0, v27
	v_rcp_f32_e32 v25, v25
	v_mul_f32_e32 v24, v24, v22
	v_fmamk_f32 v22, v65, 0x39800000, v13
	v_med3_f32 v22, v22, s50, v190
	v_fma_f32 v22, v22, 4.0, 4.0
	v_mul_f32_e32 v25, v26, v25
	v_mul_f32_e32 v25, v22, v25
	v_fmamk_f32 v22, v50, 0x39800000, v6
	v_min_f32_e32 v22, 0x40e00000, v22
	v_mul_f32_e32 v27, 0xc01d265f, v22
	v_exp_f32_e32 v27, v27
	v_fmamk_f32 v28, v51, 0x39800000, v7
	v_min_f32_e32 v28, 0x40e00000, v28
	v_mul_f32_e32 v29, 0xc01d265f, v28
	v_add_f32_e32 v27, 1.0, v27
	v_rcp_f32_e32 v27, v27
	v_exp_f32_e32 v29, v29
	v_fmamk_f32 v26, v54, 0x39800000, v2
	v_med3_f32 v26, v26, s50, v190
	v_fma_f32 v26, v26, 4.0, 4.0
	v_mul_f32_e32 v22, v22, v27
	v_add_f32_e32 v27, 1.0, v29
	v_rcp_f32_e32 v27, v27
	v_mul_f32_e32 v26, v26, v22
	v_fmamk_f32 v22, v55, 0x39800000, v3
	v_med3_f32 v22, v22, s50, v190
	v_fma_f32 v22, v22, 4.0, 4.0
	v_mul_f32_e32 v27, v28, v27
	v_mul_f32_e32 v27, v22, v27
	v_fmamk_f32 v22, v52, 0x39800000, v8
	v_min_f32_e32 v22, 0x40e00000, v22
	v_mul_f32_e32 v29, 0xc01d265f, v22
	v_exp_f32_e32 v29, v29
	v_fmamk_f32 v30, v53, 0x39800000, v9
	v_min_f32_e32 v30, 0x40e00000, v30
	v_mul_f32_e32 v31, 0xc01d265f, v30
	v_add_f32_e32 v29, 1.0, v29
	v_rcp_f32_e32 v29, v29
	v_exp_f32_e32 v31, v31
	v_fmamk_f32 v28, v56, 0x39800000, v4
	v_med3_f32 v28, v28, s50, v190
	v_mul_f32_e32 v22, v22, v29
	v_add_f32_e32 v29, 1.0, v31
	v_rcp_f32_e32 v29, v29
	v_fma_f32 v28, v28, 4.0, 4.0
	v_mul_f32_e32 v28, v28, v22
	v_fmamk_f32 v22, v57, 0x39800000, v5
	v_mul_f32_e32 v29, v30, v29
	v_mov_b32_e32 v30, v24
	v_med3_f32 v22, v22, s50, v190
	v_mov_b32_e32 v31, v25
	v_cvt_pk_fp8_f32 v24, v21, v23
	v_mov_b32_e32 v21, v26
	v_mov_b32_e32 v23, v27
	v_fma_f32 v22, v22, 4.0, 4.0
	v_cvt_pk_fp8_f32 v25, v21, v23
	v_mul_f32_e32 v29, v22, v29
	v_fmamk_f32 v14, v42, 0x39800000, v14
	v_mov_b32_e32 v21, v28
	v_mov_b32_e32 v23, v29
	v_min_f32_e32 v14, 0x40e00000, v14
	v_cvt_pk_fp8_f32 v25, v21, v23 op_sel:[0,0,1]
	v_mul_f32_e32 v21, 0xc01d265f, v14
	v_add_u32_e32 v22, 0xa0, v20
	v_cvt_pk_fp8_f32 v24, v30, v31 op_sel:[0,0,1]
	v_ashrrev_i32_e32 v23, 31, v22
	v_exp_f32_e32 v21, v21
	v_lshlrev_b64 v[22:23], 11, v[22:23]
	v_lshl_add_u64 v[22:23], s[74:75], 0, v[22:23]
	v_fmamk_f32 v15, v43, 0x39800000, v15
	v_lshl_add_u64 v[22:23], v[22:23], 0, v[18:19]
	v_min_f32_e32 v15, 0x40e00000, v15
	global_store_dwordx2 v[22:23], v[24:25], off
	v_add_f32_e32 v21, 1.0, v21
	v_mul_f32_e32 v22, 0xc01d265f, v15
	v_rcp_f32_e32 v21, v21
	v_fmamk_f32 v10, v46, 0x39800000, v10
	v_exp_f32_e32 v22, v22
	v_med3_f32 v10, v10, s50, v190
	v_fma_f32 v10, v10, 4.0, 4.0
	v_mul_f32_e32 v14, v14, v21
	v_mul_f32_e32 v10, v10, v14
	v_add_f32_e32 v14, 1.0, v22
	v_rcp_f32_e32 v14, v14
	v_fmamk_f32 v11, v47, 0x39800000, v11
	v_med3_f32 v11, v11, s50, v190
	v_fma_f32 v11, v11, 4.0, 4.0
	v_mul_f32_e32 v14, v15, v14
	v_mul_f32_e32 v11, v11, v14
	v_fmamk_f32 v14, v44, 0x39800000, v16
	v_min_f32_e32 v14, 0x40e00000, v14
	v_mul_f32_e32 v15, 0xc01d265f, v14
	v_exp_f32_e32 v15, v15
	v_fmac_f32_e32 v17, 0x39800000, v45
	v_min_f32_e32 v16, 0x40e00000, v17
	v_mul_f32_e32 v17, 0xc01d265f, v16
	v_add_f32_e32 v15, 1.0, v15
	v_rcp_f32_e32 v15, v15
	v_fmamk_f32 v12, v48, 0x39800000, v12
	v_exp_f32_e32 v17, v17
	v_med3_f32 v12, v12, s50, v190
	v_fma_f32 v12, v12, 4.0, 4.0
	v_mul_f32_e32 v14, v14, v15
	v_mul_f32_e32 v12, v12, v14
	v_add_f32_e32 v14, 1.0, v17
	v_rcp_f32_e32 v14, v14
	v_fmac_f32_e32 v13, 0x39800000, v49
	v_med3_f32 v13, v13, s50, v190
	v_fma_f32 v13, v13, 4.0, 4.0
	v_fmamk_f32 v6, v38, 0x39800000, v6
	v_mul_f32_e32 v14, v16, v14
	v_min_f32_e32 v6, 0x40e00000, v6
	v_mul_f32_e32 v13, v13, v14
	v_mul_f32_e32 v14, 0xc01d265f, v6
	v_exp_f32_e32 v14, v14
	v_fmamk_f32 v7, v39, 0x39800000, v7
	v_min_f32_e32 v7, 0x40e00000, v7
	v_mul_f32_e32 v15, 0xc01d265f, v7
	v_add_f32_e32 v14, 1.0, v14
	v_rcp_f32_e32 v14, v14
	v_fmamk_f32 v2, v34, 0x39800000, v2
	v_exp_f32_e32 v15, v15
	v_med3_f32 v2, v2, s50, v190
	v_fma_f32 v2, v2, 4.0, 4.0
	v_mul_f32_e32 v6, v6, v14
	v_mul_f32_e32 v6, v2, v6
	v_fmamk_f32 v2, v35, 0x39800000, v3
	v_add_f32_e32 v3, 1.0, v15
	v_rcp_f32_e32 v3, v3
	v_med3_f32 v2, v2, s50, v190
	v_fma_f32 v2, v2, 4.0, 4.0
	v_mul_f32_e32 v3, v7, v3
	v_mul_f32_e32 v3, v2, v3
	v_fmamk_f32 v2, v40, 0x39800000, v8
	v_min_f32_e32 v2, 0x40e00000, v2
	v_mul_f32_e32 v7, 0xc01d265f, v2
	v_exp_f32_e32 v7, v7
	v_fmac_f32_e32 v9, 0x39800000, v41
	v_min_f32_e32 v8, 0x40e00000, v9
	v_mul_f32_e32 v9, 0xc01d265f, v8
	v_add_f32_e32 v7, 1.0, v7
	v_rcp_f32_e32 v7, v7
	v_fmamk_f32 v4, v36, 0x39800000, v4
	v_exp_f32_e32 v9, v9
	v_med3_f32 v4, v4, s50, v190
	v_fma_f32 v4, v4, 4.0, 4.0
	v_mul_f32_e32 v2, v2, v7
	v_mul_f32_e32 v7, v4, v2
	v_add_f32_e32 v2, 1.0, v9
	v_rcp_f32_e32 v2, v2
	v_fmac_f32_e32 v5, 0x39800000, v37
	v_med3_f32 v4, v5, s50, v190
	v_fma_f32 v4, v4, 4.0, 4.0
	v_mul_f32_e32 v2, v8, v2
	v_mul_f32_e32 v8, v4, v2
	v_mov_b32_e32 v5, v10
	v_mov_b32_e32 v9, v11
	v_cvt_pk_fp8_f32 v4, v5, v9
	v_cvt_pk_fp8_f32 v5, v6, v3
	v_add_u32_e32 v2, 0xb0, v20
	v_mov_b32_e32 v10, v12
	v_mov_b32_e32 v11, v13
	v_mov_b32_e32 v3, v7
	v_mov_b32_e32 v6, v8
	v_cvt_pk_fp8_f32 v4, v10, v11 op_sel:[0,0,1]
	v_cvt_pk_fp8_f32 v5, v3, v6 op_sel:[0,0,1]
	v_ashrrev_i32_e32 v3, 31, v2
	v_lshlrev_b64 v[2:3], 11, v[2:3]
	v_lshl_add_u64 v[2:3], s[74:75], 0, v[2:3]
	v_lshl_add_u64 v[2:3], v[2:3], 0, v[18:19]
	global_store_dwordx2 v[2:3], v[4:5], off
	s_cbranch_vccnz .LBB0_2527
	s_mov_b32 s6, s4
	s_mov_b32 s7, s4
	s_mov_b32 s5, s4
	v_mov_b64_e32 v[36:37], s[6:7]
	v_mov_b64_e32 v[160:161], s[6:7]
	v_mov_b64_e32 v[148:149], s[6:7]
	v_mov_b64_e32 v[140:141], s[6:7]
	v_mov_b64_e32 v[132:133], s[6:7]
	v_mov_b64_e32 v[124:125], s[6:7]
	v_mov_b64_e32 v[116:117], s[6:7]
	v_mov_b64_e32 v[108:109], s[6:7]
	v_mov_b64_e32 v[100:101], s[6:7]
	v_mov_b64_e32 v[156:157], s[6:7]
	v_mov_b64_e32 v[152:153], s[6:7]
	v_mov_b64_e32 v[144:145], s[6:7]
	v_mov_b64_e32 v[136:137], s[6:7]
	v_mov_b64_e32 v[128:129], s[6:7]
	v_mov_b64_e32 v[120:121], s[6:7]
	v_mov_b64_e32 v[112:113], s[6:7]
	v_mov_b64_e32 v[104:105], s[6:7]
	v_mov_b64_e32 v[92:93], s[6:7]
	v_mov_b64_e32 v[84:85], s[6:7]
	v_mov_b64_e32 v[76:77], s[6:7]
	v_mov_b64_e32 v[68:69], s[6:7]
	v_mov_b64_e32 v[60:61], s[6:7]
	v_mov_b64_e32 v[52:53], s[6:7]
	v_mov_b64_e32 v[44:45], s[6:7]
	v_mov_b64_e32 v[40:41], s[6:7]
	v_mov_b64_e32 v[96:97], s[6:7]
	v_mov_b64_e32 v[88:89], s[6:7]
	v_mov_b64_e32 v[80:81], s[6:7]
	v_mov_b64_e32 v[72:73], s[6:7]
	v_mov_b64_e32 v[64:65], s[6:7]
	v_mov_b64_e32 v[56:57], s[6:7]
	v_mov_b64_e32 v[48:49], s[6:7]
	v_mov_b64_e32 v[34:35], s[4:5]
	v_mov_b64_e32 v[158:159], s[4:5]
	v_mov_b64_e32 v[146:147], s[4:5]
	v_mov_b64_e32 v[138:139], s[4:5]
	v_mov_b64_e32 v[130:131], s[4:5]
	v_mov_b64_e32 v[122:123], s[4:5]
	v_mov_b64_e32 v[114:115], s[4:5]
	v_mov_b64_e32 v[106:107], s[4:5]
	v_mov_b64_e32 v[98:99], s[4:5]
	v_mov_b64_e32 v[154:155], s[4:5]
	v_mov_b64_e32 v[150:151], s[4:5]
	v_mov_b64_e32 v[142:143], s[4:5]
	v_mov_b64_e32 v[134:135], s[4:5]
	v_mov_b64_e32 v[126:127], s[4:5]
	v_mov_b64_e32 v[118:119], s[4:5]
	v_mov_b64_e32 v[110:111], s[4:5]
	v_mov_b64_e32 v[102:103], s[4:5]
	v_mov_b64_e32 v[90:91], s[4:5]
	v_mov_b64_e32 v[82:83], s[4:5]
	v_mov_b64_e32 v[74:75], s[4:5]
	v_mov_b64_e32 v[66:67], s[4:5]
	v_mov_b64_e32 v[58:59], s[4:5]
	v_mov_b64_e32 v[50:51], s[4:5]
	v_mov_b64_e32 v[42:43], s[4:5]
	v_mov_b64_e32 v[38:39], s[4:5]
	v_mov_b64_e32 v[94:95], s[4:5]
	v_mov_b64_e32 v[86:87], s[4:5]
	v_mov_b64_e32 v[78:79], s[4:5]
	v_mov_b64_e32 v[70:71], s[4:5]
	v_mov_b64_e32 v[62:63], s[4:5]
	v_mov_b64_e32 v[54:55], s[4:5]
	v_mov_b64_e32 v[46:47], s[4:5]
	s_andn2_b64 vcc, exec, s[8:9]
	s_cbranch_vccnz .LBB0_2526
	s_barrier
	s_branch .LBB0_2526
